# sliding-window attention phase rewritten by hand: raw-q MFMA with f32 row scale, fixed-shift exp2 softmax (no row-max pass), unrolled 8 query tiles, batched LDS fragment reads
# speedup vs baseline: 1.0067x; 1.0023x over previous
.LBB0_1391:
	s_cmp_lt_i32 s46, 15
	s_cselect_b64 s[2:3], -1, 0
	s_and_b64 s[28:29], s[2:3], s[6:7]
	s_andn2_b64 vcc, exec, s[28:29]
	s_cbranch_vccnz .LBB0_1473
	s_mov_b64 s[2:3], s[0:1]
	s_load_dwordx2 s[12:13], s[2:3], 0xc8
	v_and_b32_e32 v1, 0x7f, v0
	s_getpc_b64 s[4:5]
	s_add_u32 s4, s4, _ZL9T5_BUCKET@rel32@lo+4
	s_addc_u32 s5, s5, _ZL9T5_BUCKET@rel32@hi+12
	s_waitcnt lgkmcnt(0)
	global_load_ubyte v1, v1, s[4:5]
	s_load_dwordx4 s[8:11], s[2:3], 0x48
	s_load_dwordx4 s[24:27], s[2:3], 0x68
	s_waitcnt vmcnt(0)
	v_lshrrev_b32_e32 v2, 7, v0
	v_or_b32_e32 v3, 0x200, v0
	v_or_b32_e32 v4, 0x400, v0
	v_or_b32_e32 v5, 0x600, v0
	v_or_b32_e32 v6, 0x800, v0
	v_or_b32_e32 v7, 0xa00, v0
	v_or_b32_e32 v8, 0xc00, v0
	v_lshrrev_b32_e32 v3, 7, v3
	v_lshrrev_b32_e32 v9, 7, v4
	v_lshrrev_b32_e32 v5, 7, v5
	v_lshrrev_b32_e32 v10, 7, v6
	v_lshrrev_b32_e32 v7, 7, v7
	v_lshrrev_b32_e32 v11, 7, v8
	s_add_i32 s3, 0, 0x11400
	s_movk_i32 s4, 0xe00
	v_readfirstlane_b32 s2, v0
	v_cmp_gt_u32_e32 vcc, s4, v8
	v_lshlrev_b32_e32 v1, 5, v1
	v_or_b32_e32 v2, v2, v1
	v_or_b32_e32 v3, v3, v1
	v_or_b32_e32 v9, v9, v1
	v_or_b32_e32 v5, v5, v1
	v_or_b32_e32 v10, v10, v1
	v_or_b32_e32 v7, v7, v1
	v_or_b32_e32 v11, v11, v1
	v_lshlrev_b32_e32 v2, 2, v2
	v_lshlrev_b32_e32 v3, 2, v3
	v_lshlrev_b32_e32 v9, 2, v9
	v_lshlrev_b32_e32 v5, 2, v5
	v_lshlrev_b32_e32 v10, 2, v10
	v_lshlrev_b32_e32 v7, 2, v7
	v_lshlrev_b32_e32 v11, 2, v11
	s_waitcnt lgkmcnt(0)
	global_load_dword v12, v2, s[10:11]
	global_load_dword v13, v3, s[10:11]
	global_load_dword v14, v9, s[10:11]
	global_load_dword v15, v5, s[10:11]
	global_load_dword v16, v10, s[10:11]
	global_load_dword v17, v7, s[10:11]
	global_load_dword v18, v11, s[10:11]
	v_lshl_add_u32 v2, v0, 2, s3
	v_lshl_add_u32 v3, v4, 2, s3
	v_lshl_add_u32 v4, v6, 2, s3
	v_lshl_add_u32 v5, v8, 2, s3
	s_waitcnt vmcnt(6)
	v_mul_f32_e32 v6, 0x3fb8aa3b, v12
	v_add_f32_e32 v6, 0xc1800000, v6
	s_waitcnt vmcnt(5)
	v_mul_f32_e32 v7, 0x3fb8aa3b, v13
	v_add_f32_e32 v7, 0xc1800000, v7
	s_waitcnt vmcnt(4)
	v_mul_f32_e32 v9, 0x3fb8aa3b, v14
	v_add_f32_e32 v9, 0xc1800000, v9
	s_waitcnt vmcnt(3)
	v_mul_f32_e32 v10, 0x3fb8aa3b, v15
	v_add_f32_e32 v10, 0xc1800000, v10
	s_waitcnt vmcnt(2)
	v_mul_f32_e32 v11, 0x3fb8aa3b, v16
	v_add_f32_e32 v11, 0xc1800000, v11
	s_waitcnt vmcnt(1)
	v_mul_f32_e32 v12, 0x3fb8aa3b, v17
	v_add_f32_e32 v12, 0xc1800000, v12
	s_waitcnt vmcnt(0)
	v_mul_f32_e32 v13, 0x3fb8aa3b, v18
	v_add_f32_e32 v13, 0xc1800000, v13
	ds_write2st64_b32 v2, v6, v7 offset1:8
	ds_write_b32 v3, v9
	ds_write_b32 v4, v11
	ds_write2st64_b32 v2, v10, v12 offset0:24 offset1:40
	ds_write_b32 v5, v13
	s_and_saveexec_b64 s[6:7], vcc
	s_cbranch_execz .LBB0_1394
	v_or_b32_e32 v3, 0xe00, v0
	v_lshrrev_b32_e32 v3, 7, v3
	v_add_lshl_u32 v1, v3, v1, 2
	global_load_dword v1, v1, s[10:11]
	s_waitcnt vmcnt(0)
	v_mul_f32_e32 v1, 0x3fb8aa3b, v1
	v_add_f32_e32 v1, 0xc1800000, v1
	ds_write_b32 v2, v1 offset:14336

.LBB0_1396:
	s_or_b64 exec, exec, s[6:7]
	s_add_u32 s14, s12, 0x18000000
	s_addc_u32 s15, s13, 0
	s_add_u32 s16, s12, 0x2a000000
	s_addc_u32 s17, s13, 0
	s_add_u32 s30, s12, 0x22000000
	s_addc_u32 s31, s13, 0
	v_readfirstlane_b32 s33, v0
	v_and_b32_e32 v2, 15, v242
	v_lshrrev_b32_e32 v3, 4, v242
	s_lshr_b32 s33, s33, 6
	v_lshrrev_b32_e32 v232, 1, v0
	v_and_b32_e32 v233, 1, v0
	v_mul_u32_u24_e32 v4, 0x90, v232
	v_lshl_add_u32 v4, v233, 6, v4
	v_mul_u32_u24_e32 v6, 0x1400, v232
	v_lshl_add_u32 v6, v233, 6, v6
	v_lshlrev_b32_e32 v234, 7, v233
	v_add_u32_e32 v19, 0x15400, v234
	v_lshrrev_b32_e32 v232, 3, v0
	v_and_b32_e32 v233, 7, v0
	v_mul_u32_u24_e32 v5, 0x210, v232
	v_lshl_add_u32 v5, v233, 4, v5
	v_add_u32_e32 v5, 0x9000, v5
	v_lshlrev_b32_e32 v7, 15, v232
	v_lshl_add_u32 v7, v233, 4, v7
	v_mul_u32_u24_e32 v8, 0x1400, v2
	v_lshl_add_u32 v8, v3, 4, v8
	v_lshlrev_b32_e32 v9, 12, v2
	v_lshl_add_u32 v9, v3, 3, v9
	v_mul_u32_u24_e32 v10, 0x90, v2
	v_lshl_add_u32 v10, v3, 4, v10
	v_mul_u32_u24_e32 v11, 0x210, v2
	v_lshl_add_u32 v11, v3, 3, v11
	v_add_u32_e32 v11, 0x9000, v11
	v_add_u32_e32 v12, 0x2100, v11
	v_add_u32_e32 v13, 0x4200, v11
	v_add_u32_e32 v14, 0x6300, v11
	v_xor_b32_e32 v15, 16, v242
	v_lshlrev_b32_e32 v15, 2, v15
	v_xor_b32_e32 v16, 32, v242
	v_lshlrev_b32_e32 v16, 2, v16
	v_xor_b32_e32 v17, 1, v242
	v_lshlrev_b32_e32 v17, 2, v17
	v_lshlrev_b32_e32 v232, 2, v3
	v_sub_u32_e32 v18, v2, v232
	v_add_u32_e32 v18, 0x80, v18
	v_mov_b32_e32 v89, 0xff800000
	v_mov_b32_e32 v90, 0
	s_mov_b32 s34, s96
	s_waitcnt lgkmcnt(0)
	s_barrier
	s_cmpk_gt_u32 s34, 0x3ff
	s_cbranch_scc1 .Lat_done
	s_and_b32 s3, s34, 3
	s_bfe_u32 s4, s34, 0x70002
	s_lshr_b32 s5, s34, 9
	s_lshl_b32 s6, s5, 14
	s_lshl_b32 s7, s4, 7
	s_add_i32 s6, s6, s7
	s_sub_i32 s6, s6, 0x80
	s_mul_i32 s7, s6, 0x1400
	s_ashr_i32 s9, s7, 31
	s_add_u32 s40, s14, s7
	s_addc_u32 s41, s15, s9
	s_lshl_b32 s7, s3, 7
	s_add_u32 s40, s40, s7
	s_addc_u32 s41, s41, 0
	s_lshl_b32 s6, s5, 2
	s_add_i32 s6, s6, s3
	s_lshl_b32 s6, s6, 21
	s_lshl_b32 s7, s4, 8
	s_sub_i32 s7, s7, 0x100
	s_add_i32 s6, s6, s7
	s_ashr_i32 s7, s6, 31
	s_add_u32 s42, s16, s6
	s_addc_u32 s43, s17, s7
	global_load_dwordx4 v[20:23], v6, s[40:41] offset:0
	global_load_dwordx4 v[24:27], v6, s[40:41] offset:16
	global_load_dwordx4 v[28:31], v6, s[40:41] offset:32
	global_load_dwordx4 v[32:35], v6, s[40:41] offset:48
	global_load_dwordx4 v[36:39], v7, s[42:43] offset:0
	global_load_dwordx4 v[40:43], v7, s[42:43] offset:128
	global_load_dwordx4 v[44:47], v7, s[42:43] offset:256
	global_load_dwordx4 v[48:51], v7, s[42:43] offset:384
.Lat_item:
	s_and_b32 s35, s34, 3
	s_bfe_u32 s36, s34, 0x70002
	s_lshr_b32 s37, s34, 9
	s_lshl_b32 s38, s35, 3
	s_add_i32 s38, s38, s33
	ds_read_b128 v[160:163], v19 offset:0
	ds_read_b128 v[164:167], v19 offset:16
	ds_read_b128 v[168:171], v19 offset:32
	ds_read_b128 v[172:175], v19 offset:48
	ds_read_b128 v[176:179], v19 offset:64
	ds_read_b128 v[180:183], v19 offset:80
	ds_read_b128 v[184:187], v19 offset:96
	ds_read_b128 v[188:191], v19 offset:112
	s_waitcnt vmcnt(0)
	s_cmp_lg_u32 s36, 0
	s_cbranch_scc1 .Lat_nz
	s_mov_b64 s[2:3], exec
	v_cmp_gt_u32_e32 vcc, 0x100, v0
	s_and_b64 exec, exec, vcc
	v_mov_b32_e32 v20, 0
	v_mov_b32_e32 v21, 0
	v_mov_b32_e32 v22, 0
	v_mov_b32_e32 v23, 0
	v_mov_b32_e32 v24, 0
	v_mov_b32_e32 v25, 0
	v_mov_b32_e32 v26, 0
	v_mov_b32_e32 v27, 0
	v_mov_b32_e32 v28, 0
	v_mov_b32_e32 v29, 0
	v_mov_b32_e32 v30, 0
	v_mov_b32_e32 v31, 0
	v_mov_b32_e32 v32, 0
	v_mov_b32_e32 v33, 0
	v_mov_b32_e32 v34, 0
	v_mov_b32_e32 v35, 0
	s_mov_b64 exec, s[2:3]
	v_mov_b32_e32 v36, 0
	v_mov_b32_e32 v37, 0
	v_mov_b32_e32 v38, 0
	v_mov_b32_e32 v39, 0
	v_mov_b32_e32 v40, 0
	v_mov_b32_e32 v41, 0
	v_mov_b32_e32 v42, 0
	v_mov_b32_e32 v43, 0
.Lat_nz:
	v_lshlrev_b32_e32 v108, 16, v20
	v_and_b32_e32 v109, 0xffff0000, v20
	v_lshlrev_b32_e32 v110, 16, v21
	v_and_b32_e32 v111, 0xffff0000, v21
	v_lshlrev_b32_e32 v112, 16, v22
	v_and_b32_e32 v113, 0xffff0000, v22
	v_lshlrev_b32_e32 v114, 16, v23
	v_and_b32_e32 v115, 0xffff0000, v23
	v_lshlrev_b32_e32 v116, 16, v24
	v_and_b32_e32 v117, 0xffff0000, v24
	v_lshlrev_b32_e32 v118, 16, v25
	v_and_b32_e32 v119, 0xffff0000, v25
	v_lshlrev_b32_e32 v120, 16, v26
	v_and_b32_e32 v121, 0xffff0000, v26
	v_lshlrev_b32_e32 v122, 16, v27
	v_and_b32_e32 v123, 0xffff0000, v27
	v_lshlrev_b32_e32 v124, 16, v28
	v_and_b32_e32 v125, 0xffff0000, v28
	v_lshlrev_b32_e32 v126, 16, v29
	v_and_b32_e32 v127, 0xffff0000, v29
	v_lshlrev_b32_e32 v128, 16, v30
	v_and_b32_e32 v129, 0xffff0000, v30
	v_lshlrev_b32_e32 v130, 16, v31
	v_and_b32_e32 v131, 0xffff0000, v31
	v_lshlrev_b32_e32 v132, 16, v32
	v_and_b32_e32 v133, 0xffff0000, v32
	v_lshlrev_b32_e32 v134, 16, v33
	v_and_b32_e32 v135, 0xffff0000, v33
	v_lshlrev_b32_e32 v136, 16, v34
	v_and_b32_e32 v137, 0xffff0000, v34
	v_lshlrev_b32_e32 v138, 16, v35
	v_and_b32_e32 v139, 0xffff0000, v35
	v_pk_mul_f32 v[232:233], v[108:109], v[108:109]
	v_pk_fma_f32 v[232:233], v[110:111], v[110:111], v[232:233]
	v_pk_fma_f32 v[232:233], v[112:113], v[112:113], v[232:233]
	v_pk_fma_f32 v[232:233], v[114:115], v[114:115], v[232:233]
	v_pk_fma_f32 v[232:233], v[116:117], v[116:117], v[232:233]
	v_pk_fma_f32 v[232:233], v[118:119], v[118:119], v[232:233]
	v_pk_fma_f32 v[232:233], v[120:121], v[120:121], v[232:233]
	v_pk_fma_f32 v[232:233], v[122:123], v[122:123], v[232:233]
	v_pk_fma_f32 v[232:233], v[124:125], v[124:125], v[232:233]
	v_pk_fma_f32 v[232:233], v[126:127], v[126:127], v[232:233]
	v_pk_fma_f32 v[232:233], v[128:129], v[128:129], v[232:233]
	v_pk_fma_f32 v[232:233], v[130:131], v[130:131], v[232:233]
	v_pk_fma_f32 v[232:233], v[132:133], v[132:133], v[232:233]
	v_pk_fma_f32 v[232:233], v[134:135], v[134:135], v[232:233]
	v_pk_fma_f32 v[232:233], v[136:137], v[136:137], v[232:233]
	v_pk_fma_f32 v[232:233], v[138:139], v[138:139], v[232:233]
	s_nop 0
	v_add_f32_e32 v232, v232, v233
	s_barrier
	ds_bpermute_b32 v233, v17, v232
	s_waitcnt lgkmcnt(0)
	v_add_f32_e32 v232, v232, v233
	v_mul_f32_e32 v232, 0x3c800000, v232
	v_add_f32_e32 v232, 0x358637bd, v232
	v_rsq_f32_e32 v232, v232
	s_nop 0
	v_mul_f32_e32 v108, v108, v232
	v_mul_f32_e32 v109, v109, v232
	v_mul_f32_e32 v110, v110, v232
	v_mul_f32_e32 v111, v111, v232
	v_mul_f32_e32 v112, v112, v232
	v_mul_f32_e32 v113, v113, v232
	v_mul_f32_e32 v114, v114, v232
	v_mul_f32_e32 v115, v115, v232
	v_mul_f32_e32 v116, v116, v232
	v_mul_f32_e32 v117, v117, v232
	v_mul_f32_e32 v118, v118, v232
	v_mul_f32_e32 v119, v119, v232
	v_mul_f32_e32 v120, v120, v232
	v_mul_f32_e32 v121, v121, v232
	v_mul_f32_e32 v122, v122, v232
	v_mul_f32_e32 v123, v123, v232
	v_mul_f32_e32 v124, v124, v232
	v_mul_f32_e32 v125, v125, v232
	v_mul_f32_e32 v126, v126, v232
	v_mul_f32_e32 v127, v127, v232
	v_mul_f32_e32 v128, v128, v232
	v_mul_f32_e32 v129, v129, v232
	v_mul_f32_e32 v130, v130, v232
	v_mul_f32_e32 v131, v131, v232
	v_mul_f32_e32 v132, v132, v232
	v_mul_f32_e32 v133, v133, v232
	v_mul_f32_e32 v134, v134, v232
	v_mul_f32_e32 v135, v135, v232
	v_mul_f32_e32 v136, v136, v232
	v_mul_f32_e32 v137, v137, v232
	v_mul_f32_e32 v138, v138, v232
	v_mul_f32_e32 v139, v139, v232
	v_mul_f32_e32 v108, v108, v160
	v_mul_f32_e32 v109, v109, v161
	v_mul_f32_e32 v110, v110, v162
	v_mul_f32_e32 v111, v111, v163
	v_mul_f32_e32 v112, v112, v164
	v_mul_f32_e32 v113, v113, v165
	v_mul_f32_e32 v114, v114, v166
	v_mul_f32_e32 v115, v115, v167
	v_mul_f32_e32 v116, v116, v168
	v_mul_f32_e32 v117, v117, v169
	v_mul_f32_e32 v118, v118, v170
	v_mul_f32_e32 v119, v119, v171
	v_mul_f32_e32 v120, v120, v172
	v_mul_f32_e32 v121, v121, v173
	v_mul_f32_e32 v122, v122, v174
	v_mul_f32_e32 v123, v123, v175
	v_mul_f32_e32 v124, v124, v176
	v_mul_f32_e32 v125, v125, v177
	v_mul_f32_e32 v126, v126, v178
	v_mul_f32_e32 v127, v127, v179
	v_mul_f32_e32 v128, v128, v180
	v_mul_f32_e32 v129, v129, v181
	v_mul_f32_e32 v130, v130, v182
	v_mul_f32_e32 v131, v131, v183
	v_mul_f32_e32 v132, v132, v184
	v_mul_f32_e32 v133, v133, v185
	v_mul_f32_e32 v134, v134, v186
	v_mul_f32_e32 v135, v135, v187
	v_mul_f32_e32 v136, v136, v188
	v_mul_f32_e32 v137, v137, v189
	v_mul_f32_e32 v138, v138, v190
	v_mul_f32_e32 v139, v139, v191
	v_cvt_pk_bf16_f32 v20, v108, v109
	v_cvt_pk_bf16_f32 v21, v110, v111
	v_cvt_pk_bf16_f32 v22, v112, v113
	v_cvt_pk_bf16_f32 v23, v114, v115
	v_cvt_pk_bf16_f32 v24, v116, v117
	v_cvt_pk_bf16_f32 v25, v118, v119
	v_cvt_pk_bf16_f32 v26, v120, v121
	v_cvt_pk_bf16_f32 v27, v122, v123
	v_cvt_pk_bf16_f32 v28, v124, v125
	v_cvt_pk_bf16_f32 v29, v126, v127
	v_cvt_pk_bf16_f32 v30, v128, v129
	v_cvt_pk_bf16_f32 v31, v130, v131
	v_cvt_pk_bf16_f32 v32, v132, v133
	v_cvt_pk_bf16_f32 v33, v134, v135
	v_cvt_pk_bf16_f32 v34, v136, v137
	v_cvt_pk_bf16_f32 v35, v138, v139
	ds_write_b128 v4, v[20:23] offset:0
	ds_write_b128 v4, v[24:27] offset:16
	ds_write_b128 v4, v[28:31] offset:32
	ds_write_b128 v4, v[32:35] offset:48
	ds_write_b128 v5, v[36:39] offset:0
	ds_write_b128 v5, v[40:43] offset:128
	ds_write_b128 v5, v[44:47] offset:256
	ds_write_b128 v5, v[48:51] offset:384
	s_lshl_b32 s2, s37, 14
	s_lshl_b32 s3, s36, 7
	s_add_i32 s2, s2, s3
	s_mul_hi_u32 s5, s2, 0x1400
	s_mul_i32 s4, s2, 0x1400
	s_add_u32 s48, s14, s4
	s_addc_u32 s49, s15, s5
	s_lshl_b32 s4, s38, 7
	s_add_i32 s4, s4, 0x400
	s_add_u32 s48, s48, s4
	s_addc_u32 s49, s49, 0
	s_lshr_b32 s5, s2, 20
	s_lshl_b32 s4, s2, 12
	s_add_u32 s50, s30, s4
	s_addc_u32 s51, s31, s5
	s_lshl_b32 s4, s38, 7
	s_add_u32 s50, s50, s4
	s_addc_u32 s51, s51, 0
	s_lshl_b32 s4, s38, 2
	s_load_dword s54, s[26:27], s4
	s_waitcnt lgkmcnt(0)
	s_barrier
	global_load_dwordx4 v[92:95], v8, s[48:49]
	global_load_dwordx4 v[96:99], v8, s[48:49] offset:64
	s_add_i32 s39, s34, s91
	s_cmpk_gt_u32 s39, 0x3ff
	s_cbranch_scc1 .Lat_nopf
	s_and_b32 s3, s39, 3
	s_bfe_u32 s4, s39, 0x70002
	s_lshr_b32 s5, s39, 9
	s_lshl_b32 s6, s5, 14
	s_lshl_b32 s7, s4, 7
	s_add_i32 s6, s6, s7
	s_sub_i32 s6, s6, 0x80
	s_mul_i32 s7, s6, 0x1400
	s_ashr_i32 s9, s7, 31
	s_add_u32 s40, s14, s7
	s_addc_u32 s41, s15, s9
	s_lshl_b32 s7, s3, 7
	s_add_u32 s40, s40, s7
	s_addc_u32 s41, s41, 0
	s_lshl_b32 s6, s5, 2
	s_add_i32 s6, s6, s3
	s_lshl_b32 s6, s6, 21
	s_lshl_b32 s7, s4, 8
	s_sub_i32 s7, s7, 0x100
	s_add_i32 s6, s6, s7
	s_ashr_i32 s7, s6, 31
	s_add_u32 s42, s16, s6
	s_addc_u32 s43, s17, s7
	global_load_dwordx4 v[20:23], v6, s[40:41] offset:0
	global_load_dwordx4 v[24:27], v6, s[40:41] offset:16
	global_load_dwordx4 v[28:31], v6, s[40:41] offset:32
	global_load_dwordx4 v[32:35], v6, s[40:41] offset:48
	global_load_dwordx4 v[36:39], v7, s[42:43] offset:0
	global_load_dwordx4 v[40:43], v7, s[42:43] offset:128
	global_load_dwordx4 v[44:47], v7, s[42:43] offset:256
	global_load_dwordx4 v[48:51], v7, s[42:43] offset:384
	s_branch .Lat_pfd
.Lat_nopf:
	global_load_dwordx4 v[20:23], v6, s[40:41] offset:0
	global_load_dwordx4 v[24:27], v6, s[40:41] offset:16
	global_load_dwordx4 v[28:31], v6, s[40:41] offset:32
	global_load_dwordx4 v[32:35], v6, s[40:41] offset:48
	global_load_dwordx4 v[36:39], v7, s[42:43] offset:0
	global_load_dwordx4 v[40:43], v7, s[42:43] offset:128
	global_load_dwordx4 v[44:47], v7, s[42:43] offset:256
	global_load_dwordx4 v[48:51], v7, s[42:43] offset:384
.Lat_pfd:
	v_mov_b32_e32 v232, s54
	v_mul_f32_e32 v232, 0x3fb8aa3b, v232
	v_add_f32_e32 v232, 0xc1800000, v232
	v_exp_f32_e32 v88, v232
	s_lshl_b32 s2, s38, 9
	s_add_i32 s2, s2, 0x11400
	v_subrev_u32_e32 v233, 0, v18
	v_and_b32_e32 v233, 0x7f, v233
	v_lshl_add_u32 v233, v233, 2, s2
	ds_read_b32 v52, v233
	v_subrev_u32_e32 v233, 1, v18
	v_and_b32_e32 v233, 0x7f, v233
	v_lshl_add_u32 v233, v233, 2, s2
	ds_read_b32 v53, v233
	v_subrev_u32_e32 v233, 2, v18
	v_and_b32_e32 v233, 0x7f, v233
	v_lshl_add_u32 v233, v233, 2, s2
	ds_read_b32 v54, v233
	v_subrev_u32_e32 v233, 3, v18
	v_and_b32_e32 v233, 0x7f, v233
	v_lshl_add_u32 v233, v233, 2, s2
	ds_read_b32 v55, v233
	v_subrev_u32_e32 v233, 16, v18
	v_and_b32_e32 v233, 0x7f, v233
	v_lshl_add_u32 v233, v233, 2, s2
	ds_read_b32 v56, v233
	v_subrev_u32_e32 v233, 17, v18
	v_and_b32_e32 v233, 0x7f, v233
	v_lshl_add_u32 v233, v233, 2, s2
	ds_read_b32 v57, v233
	v_subrev_u32_e32 v233, 18, v18
	v_and_b32_e32 v233, 0x7f, v233
	v_lshl_add_u32 v233, v233, 2, s2
	ds_read_b32 v58, v233
	v_subrev_u32_e32 v233, 19, v18
	v_and_b32_e32 v233, 0x7f, v233
	v_lshl_add_u32 v233, v233, 2, s2
	ds_read_b32 v59, v233
	v_subrev_u32_e32 v233, 32, v18
	v_and_b32_e32 v233, 0x7f, v233
	v_lshl_add_u32 v233, v233, 2, s2
	ds_read_b32 v60, v233
	v_subrev_u32_e32 v233, 33, v18
	v_and_b32_e32 v233, 0x7f, v233
	v_lshl_add_u32 v233, v233, 2, s2
	ds_read_b32 v61, v233
	v_subrev_u32_e32 v233, 34, v18
	v_and_b32_e32 v233, 0x7f, v233
	v_lshl_add_u32 v233, v233, 2, s2
	ds_read_b32 v62, v233
	v_subrev_u32_e32 v233, 35, v18
	v_and_b32_e32 v233, 0x7f, v233
	v_lshl_add_u32 v233, v233, 2, s2
	ds_read_b32 v63, v233
	s_waitcnt lgkmcnt(0)
	v_subrev_u32_e32 v233, 48, v18
	v_and_b32_e32 v233, 0x7f, v233
	v_lshl_add_u32 v233, v233, 2, s2
	ds_read_b32 v64, v233
	v_subrev_u32_e32 v233, 49, v18
	v_and_b32_e32 v233, 0x7f, v233
	v_lshl_add_u32 v233, v233, 2, s2
	ds_read_b32 v65, v233
	v_subrev_u32_e32 v233, 50, v18
	v_and_b32_e32 v233, 0x7f, v233
	v_lshl_add_u32 v233, v233, 2, s2
	ds_read_b32 v66, v233
	v_subrev_u32_e32 v233, 51, v18
	v_and_b32_e32 v233, 0x7f, v233
	v_lshl_add_u32 v233, v233, 2, s2
	ds_read_b32 v67, v233
	v_subrev_u32_e32 v233, 64, v18
	v_and_b32_e32 v233, 0x7f, v233
	v_lshl_add_u32 v233, v233, 2, s2
	ds_read_b32 v68, v233
	v_subrev_u32_e32 v233, 0x41, v18
	v_and_b32_e32 v233, 0x7f, v233
	v_lshl_add_u32 v233, v233, 2, s2
	ds_read_b32 v69, v233
	v_subrev_u32_e32 v233, 0x42, v18
	v_and_b32_e32 v233, 0x7f, v233
	v_lshl_add_u32 v233, v233, 2, s2
	ds_read_b32 v70, v233
	v_subrev_u32_e32 v233, 0x43, v18
	v_and_b32_e32 v233, 0x7f, v233
	v_lshl_add_u32 v233, v233, 2, s2
	ds_read_b32 v71, v233
	v_subrev_u32_e32 v233, 0x50, v18
	v_and_b32_e32 v233, 0x7f, v233
	v_lshl_add_u32 v233, v233, 2, s2
	ds_read_b32 v72, v233
	v_subrev_u32_e32 v233, 0x51, v18
	v_and_b32_e32 v233, 0x7f, v233
	v_lshl_add_u32 v233, v233, 2, s2
	ds_read_b32 v73, v233
	v_subrev_u32_e32 v233, 0x52, v18
	v_and_b32_e32 v233, 0x7f, v233
	v_lshl_add_u32 v233, v233, 2, s2
	ds_read_b32 v74, v233
	v_subrev_u32_e32 v233, 0x53, v18
	v_and_b32_e32 v233, 0x7f, v233
	v_lshl_add_u32 v233, v233, 2, s2
	ds_read_b32 v75, v233
	s_waitcnt lgkmcnt(0)
	v_subrev_u32_e32 v233, 0x60, v18
	v_and_b32_e32 v233, 0x7f, v233
	v_lshl_add_u32 v233, v233, 2, s2
	ds_read_b32 v76, v233
	v_subrev_u32_e32 v233, 0x61, v18
	v_and_b32_e32 v233, 0x7f, v233
	v_lshl_add_u32 v233, v233, 2, s2
	ds_read_b32 v77, v233
	v_subrev_u32_e32 v233, 0x62, v18
	v_and_b32_e32 v233, 0x7f, v233
	v_lshl_add_u32 v233, v233, 2, s2
	ds_read_b32 v78, v233
	v_subrev_u32_e32 v233, 0x63, v18
	v_and_b32_e32 v233, 0x7f, v233
	v_lshl_add_u32 v233, v233, 2, s2
	ds_read_b32 v79, v233
	v_subrev_u32_e32 v233, 0x70, v18
	v_and_b32_e32 v233, 0x7f, v233
	v_lshl_add_u32 v233, v233, 2, s2
	ds_read_b32 v80, v233
	v_subrev_u32_e32 v233, 0x71, v18
	v_and_b32_e32 v233, 0x7f, v233
	v_lshl_add_u32 v233, v233, 2, s2
	ds_read_b32 v81, v233
	v_subrev_u32_e32 v233, 0x72, v18
	v_and_b32_e32 v233, 0x7f, v233
	v_lshl_add_u32 v233, v233, 2, s2
	ds_read_b32 v82, v233
	v_subrev_u32_e32 v233, 0x73, v18
	v_and_b32_e32 v233, 0x7f, v233
	v_lshl_add_u32 v233, v233, 2, s2
	ds_read_b32 v83, v233
	v_subrev_u32_e32 v233, 0x80, v18
	v_and_b32_e32 v233, 0x7f, v233
	v_lshl_add_u32 v233, v233, 2, s2
	ds_read_b32 v84, v233
	v_subrev_u32_e32 v233, 0x81, v18
	v_and_b32_e32 v233, 0x7f, v233
	v_lshl_add_u32 v233, v233, 2, s2
	ds_read_b32 v85, v233
	v_subrev_u32_e32 v233, 0x82, v18
	v_and_b32_e32 v233, 0x7f, v233
	v_lshl_add_u32 v233, v233, 2, s2
	ds_read_b32 v86, v233
	v_subrev_u32_e32 v233, 0x83, v18
	v_and_b32_e32 v233, 0x7f, v233
	v_lshl_add_u32 v233, v233, 2, s2
	ds_read_b32 v87, v233
	s_waitcnt lgkmcnt(0)
	s_waitcnt lgkmcnt(0)
	v_mov_b32_e32 v235, 0x80
	v_subrev_u32_e32 v233, 0, v18
	v_subrev_u32_e32 v234, 1, v18
	v_cmp_gt_u32_e32 vcc, 0x80, v233
	v_cmp_lt_u32_e64 s[6:7], v234, v235
	s_nop 0
	v_cndmask_b32_e32 v52, v89, v52, vcc
	v_cndmask_b32_e64 v53, v89, v53, s[6:7]
	v_subrev_u32_e32 v233, 2, v18
	v_subrev_u32_e32 v234, 3, v18
	v_cmp_gt_u32_e32 vcc, 0x80, v233
	v_cmp_lt_u32_e64 s[6:7], v234, v235
	s_nop 0
	v_cndmask_b32_e32 v54, v89, v54, vcc
	v_cndmask_b32_e64 v55, v89, v55, s[6:7]
	v_subrev_u32_e32 v233, 16, v18
	v_subrev_u32_e32 v234, 17, v18
	v_cmp_gt_u32_e32 vcc, 0x80, v233
	v_cmp_lt_u32_e64 s[6:7], v234, v235
	s_nop 0
	v_cndmask_b32_e32 v56, v89, v56, vcc
	v_cndmask_b32_e64 v57, v89, v57, s[6:7]
	v_subrev_u32_e32 v233, 18, v18
	v_subrev_u32_e32 v234, 19, v18
	v_cmp_gt_u32_e32 vcc, 0x80, v233
	v_cmp_lt_u32_e64 s[6:7], v234, v235
	s_nop 0
	v_cndmask_b32_e32 v58, v89, v58, vcc
	v_cndmask_b32_e64 v59, v89, v59, s[6:7]
	v_subrev_u32_e32 v233, 32, v18
	v_subrev_u32_e32 v234, 33, v18
	v_cmp_gt_u32_e32 vcc, 0x80, v233
	v_cmp_lt_u32_e64 s[6:7], v234, v235
	s_nop 0
	v_cndmask_b32_e32 v60, v89, v60, vcc
	v_cndmask_b32_e64 v61, v89, v61, s[6:7]
	v_subrev_u32_e32 v233, 34, v18
	v_subrev_u32_e32 v234, 35, v18
	v_cmp_gt_u32_e32 vcc, 0x80, v233
	v_cmp_lt_u32_e64 s[6:7], v234, v235
	s_nop 0
	v_cndmask_b32_e32 v62, v89, v62, vcc
	v_cndmask_b32_e64 v63, v89, v63, s[6:7]
	v_subrev_u32_e32 v233, 48, v18
	v_subrev_u32_e32 v234, 49, v18
	v_cmp_gt_u32_e32 vcc, 0x80, v233
	v_cmp_lt_u32_e64 s[6:7], v234, v235
	s_nop 0
	v_cndmask_b32_e32 v64, v89, v64, vcc
	v_cndmask_b32_e64 v65, v89, v65, s[6:7]
	v_subrev_u32_e32 v233, 50, v18
	v_subrev_u32_e32 v234, 51, v18
	v_cmp_gt_u32_e32 vcc, 0x80, v233
	v_cmp_lt_u32_e64 s[6:7], v234, v235
	s_nop 0
	v_cndmask_b32_e32 v66, v89, v66, vcc
	v_cndmask_b32_e64 v67, v89, v67, s[6:7]
	v_subrev_u32_e32 v233, 64, v18
	v_subrev_u32_e32 v234, 0x41, v18
	v_cmp_gt_u32_e32 vcc, 0x80, v233
	v_cmp_lt_u32_e64 s[6:7], v234, v235
	s_nop 0
	v_cndmask_b32_e32 v68, v89, v68, vcc
	v_cndmask_b32_e64 v69, v89, v69, s[6:7]
	v_subrev_u32_e32 v233, 0x42, v18
	v_subrev_u32_e32 v234, 0x43, v18
	v_cmp_gt_u32_e32 vcc, 0x80, v233
	v_cmp_lt_u32_e64 s[6:7], v234, v235
	s_nop 0
	v_cndmask_b32_e32 v70, v89, v70, vcc
	v_cndmask_b32_e64 v71, v89, v71, s[6:7]
	v_subrev_u32_e32 v233, 0x50, v18
	v_subrev_u32_e32 v234, 0x51, v18
	v_cmp_gt_u32_e32 vcc, 0x80, v233
	v_cmp_lt_u32_e64 s[6:7], v234, v235
	s_nop 0
	v_cndmask_b32_e32 v72, v89, v72, vcc
	v_cndmask_b32_e64 v73, v89, v73, s[6:7]
	v_subrev_u32_e32 v233, 0x52, v18
	v_subrev_u32_e32 v234, 0x53, v18
	v_cmp_gt_u32_e32 vcc, 0x80, v233
	v_cmp_lt_u32_e64 s[6:7], v234, v235
	s_nop 0
	v_cndmask_b32_e32 v74, v89, v74, vcc
	v_cndmask_b32_e64 v75, v89, v75, s[6:7]
	v_subrev_u32_e32 v233, 0x60, v18
	v_subrev_u32_e32 v234, 0x61, v18
	v_cmp_gt_u32_e32 vcc, 0x80, v233
	v_cmp_lt_u32_e64 s[6:7], v234, v235
	s_nop 0
	v_cndmask_b32_e32 v76, v89, v76, vcc
	v_cndmask_b32_e64 v77, v89, v77, s[6:7]
	v_subrev_u32_e32 v233, 0x62, v18
	v_subrev_u32_e32 v234, 0x63, v18
	v_cmp_gt_u32_e32 vcc, 0x80, v233
	v_cmp_lt_u32_e64 s[6:7], v234, v235
	s_nop 0
	v_cndmask_b32_e32 v78, v89, v78, vcc
	v_cndmask_b32_e64 v79, v89, v79, s[6:7]
	v_subrev_u32_e32 v233, 0x70, v18
	v_subrev_u32_e32 v234, 0x71, v18
	v_cmp_gt_u32_e32 vcc, 0x80, v233
	v_cmp_lt_u32_e64 s[6:7], v234, v235
	s_nop 0
	v_cndmask_b32_e32 v80, v89, v80, vcc
	v_cndmask_b32_e64 v81, v89, v81, s[6:7]
	v_subrev_u32_e32 v233, 0x72, v18
	v_subrev_u32_e32 v234, 0x73, v18
	v_cmp_gt_u32_e32 vcc, 0x80, v233
	v_cmp_lt_u32_e64 s[6:7], v234, v235
	s_nop 0
	v_cndmask_b32_e32 v82, v89, v82, vcc
	v_cndmask_b32_e64 v83, v89, v83, s[6:7]
	v_subrev_u32_e32 v233, 0x80, v18
	v_subrev_u32_e32 v234, 0x81, v18
	v_cmp_gt_u32_e32 vcc, 0x80, v233
	v_cmp_lt_u32_e64 s[6:7], v234, v235
	s_nop 0
	v_cndmask_b32_e32 v84, v89, v84, vcc
	v_cndmask_b32_e64 v85, v89, v85, s[6:7]
	v_subrev_u32_e32 v233, 0x82, v18
	v_subrev_u32_e32 v234, 0x83, v18
	v_cmp_gt_u32_e32 vcc, 0x80, v233
	v_cmp_lt_u32_e64 s[6:7], v234, v235
	s_nop 0
	v_cndmask_b32_e32 v86, v89, v86, vcc
	v_cndmask_b32_e64 v87, v89, v87, s[6:7]
	s_add_u32 s48, s48, 0x14000
	s_addc_u32 s49, s49, 0
	ds_read_b128 v[160:163], v10 offset:0
	ds_read_b128 v[164:167], v10 offset:64
	ds_read_b128 v[168:171], v10 offset:2304
	ds_read_b128 v[172:175], v10 offset:2368
	ds_read_b128 v[176:179], v10 offset:4608
	ds_read_b128 v[180:183], v10 offset:4672
	ds_read_b128 v[184:187], v10 offset:6912
	ds_read_b128 v[188:191], v10 offset:6976
	ds_read_b128 v[192:195], v10 offset:9216
	ds_read_b128 v[196:199], v10 offset:9280
	s_waitcnt vmcnt(8)
	global_load_dwordx4 v[100:103], v8, s[48:49]
	global_load_dwordx4 v[104:107], v8, s[48:49] offset:64
	v_lshlrev_b32_e32 v234, 16, v92
	v_and_b32_e32 v235, 0xffff0000, v92
	v_pk_mul_f32 v[232:233], v[234:235], v[234:235]
	v_lshlrev_b32_e32 v234, 16, v93
	v_and_b32_e32 v235, 0xffff0000, v93
	v_pk_fma_f32 v[232:233], v[234:235], v[234:235], v[232:233]
	v_lshlrev_b32_e32 v234, 16, v94
	v_and_b32_e32 v235, 0xffff0000, v94
	v_pk_fma_f32 v[232:233], v[234:235], v[234:235], v[232:233]
	v_lshlrev_b32_e32 v234, 16, v95
	v_and_b32_e32 v235, 0xffff0000, v95
	v_pk_fma_f32 v[232:233], v[234:235], v[234:235], v[232:233]
	v_lshlrev_b32_e32 v234, 16, v96
	v_and_b32_e32 v235, 0xffff0000, v96
	v_pk_fma_f32 v[232:233], v[234:235], v[234:235], v[232:233]
	v_lshlrev_b32_e32 v234, 16, v97
	v_and_b32_e32 v235, 0xffff0000, v97
	v_pk_fma_f32 v[232:233], v[234:235], v[234:235], v[232:233]
	v_lshlrev_b32_e32 v234, 16, v98
	v_and_b32_e32 v235, 0xffff0000, v98
	v_pk_fma_f32 v[232:233], v[234:235], v[234:235], v[232:233]
	v_lshlrev_b32_e32 v234, 16, v99
	v_and_b32_e32 v235, 0xffff0000, v99
	v_pk_fma_f32 v[232:233], v[234:235], v[234:235], v[232:233]
	ds_read_b128 v[200:203], v10 offset:11520
	ds_read_b128 v[204:207], v10 offset:11584
	ds_read_b128 v[208:211], v10 offset:13824
	ds_read_b128 v[212:215], v10 offset:13888
	ds_read_b128 v[216:219], v10 offset:16128
	ds_read_b128 v[220:223], v10 offset:16192
	ds_read_b128 v[224:227], v10 offset:18432
	ds_read_b128 v[228:231], v10 offset:18496
	v_add_f32_e32 v232, v232, v233
	s_nop 0
	ds_bpermute_b32 v233, v15, v232
	s_waitcnt lgkmcnt(9)
	v_mfma_f32_16x16x32_bf16 v[108:111], v[160:163], v[92:95], 0
	v_mfma_f32_16x16x32_bf16 v[112:115], v[168:171], v[92:95], 0
	v_mfma_f32_16x16x32_bf16 v[116:119], v[176:179], v[92:95], 0
	v_mfma_f32_16x16x32_bf16 v[120:123], v[184:187], v[92:95], 0
	v_mfma_f32_16x16x32_bf16 v[124:127], v[192:195], v[92:95], 0
	v_mfma_f32_16x16x32_bf16 v[108:111], v[164:167], v[96:99], v[108:111]
	v_mfma_f32_16x16x32_bf16 v[112:115], v[172:175], v[96:99], v[112:115]
	v_mfma_f32_16x16x32_bf16 v[116:119], v[180:183], v[96:99], v[116:119]
	v_mfma_f32_16x16x32_bf16 v[120:123], v[188:191], v[96:99], v[120:123]
	v_mfma_f32_16x16x32_bf16 v[124:127], v[196:199], v[96:99], v[124:127]
	s_waitcnt lgkmcnt(0)
	v_add_f32_e32 v232, v232, v233
	v_mfma_f32_16x16x32_bf16 v[128:131], v[200:203], v[92:95], 0
	v_mfma_f32_16x16x32_bf16 v[132:135], v[208:211], v[92:95], 0
	v_mfma_f32_16x16x32_bf16 v[136:139], v[216:219], v[92:95], 0
	v_mfma_f32_16x16x32_bf16 v[140:143], v[224:227], v[92:95], 0
	ds_bpermute_b32 v233, v16, v232
	v_mfma_f32_16x16x32_bf16 v[128:131], v[204:207], v[96:99], v[128:131]
	v_mfma_f32_16x16x32_bf16 v[132:135], v[212:215], v[96:99], v[132:135]
	v_mfma_f32_16x16x32_bf16 v[136:139], v[220:223], v[96:99], v[136:139]
	v_mfma_f32_16x16x32_bf16 v[140:143], v[228:231], v[96:99], v[140:143]
	ds_read2_b64 v[160:163], v11 offset0:0 offset1:4
	ds_read2_b64 v[164:167], v12 offset0:0 offset1:4
	ds_read2_b64 v[168:171], v13 offset0:0 offset1:4
	ds_read2_b64 v[172:175], v14 offset0:0 offset1:4
	ds_read2_b64 v[176:179], v11 offset0:8 offset1:12
	ds_read2_b64 v[180:183], v12 offset0:8 offset1:12
	ds_read2_b64 v[184:187], v13 offset0:8 offset1:12
	ds_read2_b64 v[188:191], v14 offset0:8 offset1:12
	ds_read2_b64 v[192:195], v11 offset0:16 offset1:20
	ds_read2_b64 v[196:199], v12 offset0:16 offset1:20
	ds_read2_b64 v[200:203], v13 offset0:16 offset1:20
	ds_read2_b64 v[204:207], v14 offset0:16 offset1:20
	s_waitcnt lgkmcnt(12)
	v_add_f32_e32 v232, v232, v233
	v_mul_f32_e32 v232, 0x3c800000, v232
	v_add_f32_e32 v232, 0x358637bd, v232
	v_rsq_f32_e32 v236, v232
	s_nop 0
	v_mov_b32_e32 v237, v236
	s_nop 1
	v_pk_fma_f32 v[108:109], v[108:109], v[236:237], v[52:53]
	v_pk_fma_f32 v[110:111], v[110:111], v[236:237], v[54:55]
	v_pk_fma_f32 v[112:113], v[112:113], v[236:237], v[56:57]
	v_pk_fma_f32 v[114:115], v[114:115], v[236:237], v[58:59]
	v_pk_fma_f32 v[116:117], v[116:117], v[236:237], v[60:61]
	v_pk_fma_f32 v[118:119], v[118:119], v[236:237], v[62:63]
	v_pk_fma_f32 v[120:121], v[120:121], v[236:237], v[64:65]
	v_pk_fma_f32 v[122:123], v[122:123], v[236:237], v[66:67]
	v_pk_fma_f32 v[124:125], v[124:125], v[236:237], v[68:69]
	v_pk_fma_f32 v[126:127], v[126:127], v[236:237], v[70:71]
	v_pk_fma_f32 v[128:129], v[128:129], v[236:237], v[72:73]
	v_pk_fma_f32 v[130:131], v[130:131], v[236:237], v[74:75]
	v_pk_fma_f32 v[132:133], v[132:133], v[236:237], v[76:77]
	v_pk_fma_f32 v[134:135], v[134:135], v[236:237], v[78:79]
	v_pk_fma_f32 v[136:137], v[136:137], v[236:237], v[80:81]
	v_pk_fma_f32 v[138:139], v[138:139], v[236:237], v[82:83]
	v_pk_fma_f32 v[140:141], v[140:141], v[236:237], v[84:85]
	v_pk_fma_f32 v[142:143], v[142:143], v[236:237], v[86:87]
	v_exp_f32_e32 v108, v108
	v_exp_f32_e32 v109, v109
	v_exp_f32_e32 v110, v110
	v_exp_f32_e32 v111, v111
	v_exp_f32_e32 v112, v112
	v_exp_f32_e32 v113, v113
	v_exp_f32_e32 v114, v114
	v_exp_f32_e32 v115, v115
	v_exp_f32_e32 v116, v116
	v_exp_f32_e32 v117, v117
	v_exp_f32_e32 v118, v118
	v_exp_f32_e32 v119, v119
	v_exp_f32_e32 v120, v120
	v_exp_f32_e32 v121, v121
	v_exp_f32_e32 v122, v122
	v_exp_f32_e32 v123, v123
	v_exp_f32_e32 v124, v124
	v_exp_f32_e32 v125, v125
	v_exp_f32_e32 v126, v126
	v_exp_f32_e32 v127, v127
	v_exp_f32_e32 v128, v128
	v_exp_f32_e32 v129, v129
	v_exp_f32_e32 v130, v130
	v_exp_f32_e32 v131, v131
	v_exp_f32_e32 v132, v132
	v_exp_f32_e32 v133, v133
	v_exp_f32_e32 v134, v134
	v_exp_f32_e32 v135, v135
	v_exp_f32_e32 v136, v136
	v_exp_f32_e32 v137, v137
	v_exp_f32_e32 v138, v138
	v_exp_f32_e32 v139, v139
	v_exp_f32_e32 v140, v140
	v_exp_f32_e32 v141, v141
	v_exp_f32_e32 v142, v142
	v_exp_f32_e32 v143, v143
	s_cmp_lg_u32 s36, 0
	s_cbranch_scc1 .Lat_m0
	v_mov_b32_e32 v108, 0
	v_mov_b32_e32 v109, 0
	v_mov_b32_e32 v110, 0
	v_mov_b32_e32 v111, 0
	v_mov_b32_e32 v112, 0
	v_mov_b32_e32 v113, 0
	v_mov_b32_e32 v114, 0
	v_mov_b32_e32 v115, 0
	v_mov_b32_e32 v116, 0
	v_mov_b32_e32 v117, 0
	v_mov_b32_e32 v118, 0
	v_mov_b32_e32 v119, 0
	v_mov_b32_e32 v120, 0
	v_mov_b32_e32 v121, 0
	v_mov_b32_e32 v122, 0
	v_mov_b32_e32 v123, 0
	v_mov_b32_e32 v124, 0
	v_mov_b32_e32 v125, 0
	v_mov_b32_e32 v126, 0
	v_mov_b32_e32 v127, 0
	v_mov_b32_e32 v128, 0
	v_mov_b32_e32 v129, 0
	v_mov_b32_e32 v130, 0
	v_mov_b32_e32 v131, 0
	v_mov_b32_e32 v132, 0
	v_mov_b32_e32 v133, 0
	v_mov_b32_e32 v134, 0
	v_mov_b32_e32 v135, 0
	v_mov_b32_e32 v136, 0
	v_mov_b32_e32 v137, 0
	v_mov_b32_e32 v138, 0
	v_mov_b32_e32 v139, 0
.Lat_m0:
	s_nop 0
	v_pk_add_f32 v[232:233], v[108:109], v[110:111]
	v_pk_add_f32 v[234:235], v[112:113], v[114:115]
	v_pk_add_f32 v[232:233], v[232:233], v[116:117]
	v_pk_add_f32 v[234:235], v[234:235], v[118:119]
	v_pk_add_f32 v[232:233], v[232:233], v[120:121]
	v_pk_add_f32 v[234:235], v[234:235], v[122:123]
	v_pk_add_f32 v[232:233], v[232:233], v[124:125]
	v_pk_add_f32 v[234:235], v[234:235], v[126:127]
	v_pk_add_f32 v[232:233], v[232:233], v[128:129]
	v_pk_add_f32 v[234:235], v[234:235], v[130:131]
	v_pk_add_f32 v[232:233], v[232:233], v[132:133]
	v_pk_add_f32 v[234:235], v[234:235], v[134:135]
	v_pk_add_f32 v[232:233], v[232:233], v[136:137]
	v_pk_add_f32 v[234:235], v[234:235], v[138:139]
	v_pk_add_f32 v[232:233], v[232:233], v[140:141]
	v_pk_add_f32 v[234:235], v[234:235], v[142:143]
	v_pk_add_f32 v[232:233], v[232:233], v[234:235]
	s_nop 0
	v_add_f32_e32 v232, v232, v233
	v_cvt_pk_bf16_f32 v108, v108, v109
	v_cvt_pk_bf16_f32 v109, v110, v111
	v_cvt_pk_bf16_f32 v110, v112, v113
	v_cvt_pk_bf16_f32 v111, v114, v115
	v_cvt_pk_bf16_f32 v116, v116, v117
	v_cvt_pk_bf16_f32 v117, v118, v119
	v_cvt_pk_bf16_f32 v118, v120, v121
	v_cvt_pk_bf16_f32 v119, v122, v123
	v_cvt_pk_bf16_f32 v124, v124, v125
	v_cvt_pk_bf16_f32 v125, v126, v127
	v_cvt_pk_bf16_f32 v126, v128, v129
	v_cvt_pk_bf16_f32 v127, v130, v131
	v_cvt_pk_bf16_f32 v132, v132, v133
	v_cvt_pk_bf16_f32 v133, v134, v135
	v_cvt_pk_bf16_f32 v134, v136, v137
	v_cvt_pk_bf16_f32 v135, v138, v139
	v_cvt_pk_bf16_f32 v140, v140, v141
	v_cvt_pk_bf16_f32 v141, v142, v143
	v_mov_b32_e32 v142, 0
	v_mov_b32_e32 v143, 0
	ds_bpermute_b32 v233, v15, v232
	s_waitcnt lgkmcnt(1)
	v_mfma_f32_16x16x32_bf16 v[144:147], v[160:163], v[108:111], 0
	v_mfma_f32_16x16x32_bf16 v[148:151], v[164:167], v[108:111], 0
	v_mfma_f32_16x16x32_bf16 v[152:155], v[168:171], v[108:111], 0
	v_mfma_f32_16x16x32_bf16 v[156:159], v[172:175], v[108:111], 0
	v_mfma_f32_16x16x32_bf16 v[144:147], v[176:179], v[116:119], v[144:147]
	v_mfma_f32_16x16x32_bf16 v[148:151], v[180:183], v[116:119], v[148:151]
	v_mfma_f32_16x16x32_bf16 v[152:155], v[184:187], v[116:119], v[152:155]
	v_mfma_f32_16x16x32_bf16 v[156:159], v[188:191], v[116:119], v[156:159]
	v_mfma_f32_16x16x32_bf16 v[144:147], v[192:195], v[124:127], v[144:147]
	v_mfma_f32_16x16x32_bf16 v[148:151], v[196:199], v[124:127], v[148:151]
	v_mfma_f32_16x16x32_bf16 v[152:155], v[200:203], v[124:127], v[152:155]
	v_mfma_f32_16x16x32_bf16 v[156:159], v[204:207], v[124:127], v[156:159]
	ds_read2_b64 v[160:163], v11 offset0:24 offset1:28
	ds_read2_b64 v[164:167], v12 offset0:24 offset1:28
	ds_read2_b64 v[168:171], v13 offset0:24 offset1:28
	ds_read2_b64 v[172:175], v14 offset0:24 offset1:28
	ds_read2_b64 v[176:179], v11 offset0:32 offset1:32
	ds_read2_b64 v[180:183], v12 offset0:32 offset1:32
	ds_read2_b64 v[184:187], v13 offset0:32 offset1:32
	ds_read2_b64 v[188:191], v14 offset0:32 offset1:32
	s_waitcnt lgkmcnt(8)
	v_add_f32_e32 v232, v232, v233
	s_nop 0
	ds_bpermute_b32 v233, v16, v232
	s_waitcnt lgkmcnt(1)
	v_mfma_f32_16x16x32_bf16 v[144:147], v[160:163], v[132:135], v[144:147]
	v_mfma_f32_16x16x32_bf16 v[148:151], v[164:167], v[132:135], v[148:151]
	v_mfma_f32_16x16x32_bf16 v[152:155], v[168:171], v[132:135], v[152:155]
	v_mfma_f32_16x16x32_bf16 v[156:159], v[172:175], v[132:135], v[156:159]
	v_mfma_f32_16x16x32_bf16 v[144:147], v[176:179], v[140:143], v[144:147]
	v_mfma_f32_16x16x32_bf16 v[148:151], v[180:183], v[140:143], v[148:151]
	v_mfma_f32_16x16x32_bf16 v[152:155], v[184:187], v[140:143], v[152:155]
	v_mfma_f32_16x16x32_bf16 v[156:159], v[188:191], v[140:143], v[156:159]
	s_waitcnt lgkmcnt(0)
	v_add_f32_e32 v232, v232, v233
	v_add_f32_e32 v232, v232, v88
	v_rcp_f32_e32 v236, v232
	s_nop 0
	v_mov_b32_e32 v237, v236
	s_nop 4
	v_pk_mul_f32 v[144:145], v[144:145], v[236:237]
	v_pk_mul_f32 v[146:147], v[146:147], v[236:237]
	v_pk_mul_f32 v[148:149], v[148:149], v[236:237]
	v_pk_mul_f32 v[150:151], v[150:151], v[236:237]
	v_pk_mul_f32 v[152:153], v[152:153], v[236:237]
	v_pk_mul_f32 v[154:155], v[154:155], v[236:237]
	v_pk_mul_f32 v[156:157], v[156:157], v[236:237]
	v_pk_mul_f32 v[158:159], v[158:159], v[236:237]
	v_cvt_pk_bf16_f32 v144, v144, v145
	v_cvt_pk_bf16_f32 v145, v146, v147
	v_cvt_pk_bf16_f32 v148, v148, v149
	v_cvt_pk_bf16_f32 v149, v150, v151
	v_cvt_pk_bf16_f32 v152, v152, v153
	v_cvt_pk_bf16_f32 v153, v154, v155
	v_cvt_pk_bf16_f32 v156, v156, v157
	v_cvt_pk_bf16_f32 v157, v158, v159
	global_store_dwordx2 v9, v[144:145], s[50:51] offset:0
	global_store_dwordx2 v9, v[148:149], s[50:51] offset:32
	global_store_dwordx2 v9, v[152:153], s[50:51] offset:64
	global_store_dwordx2 v9, v[156:157], s[50:51] offset:96
	s_add_u32 s50, s50, 0x10000
	s_addc_u32 s51, s51, 0
	s_waitcnt vmcnt(4)
	v_mov_b32_e32 v92, v100
	v_mov_b32_e32 v93, v101
	v_mov_b32_e32 v94, v102
	v_mov_b32_e32 v95, v103
	v_mov_b32_e32 v96, v104
	v_mov_b32_e32 v97, v105
	v_mov_b32_e32 v98, v106
	v_mov_b32_e32 v99, v107
	s_add_u32 s48, s48, 0x14000
	s_addc_u32 s49, s49, 0
	ds_read_b128 v[160:163], v10 offset:2304
	ds_read_b128 v[164:167], v10 offset:2368
	ds_read_b128 v[168:171], v10 offset:4608
	ds_read_b128 v[172:175], v10 offset:4672
	ds_read_b128 v[176:179], v10 offset:6912
	ds_read_b128 v[180:183], v10 offset:6976
	ds_read_b128 v[184:187], v10 offset:9216
	ds_read_b128 v[188:191], v10 offset:9280
	ds_read_b128 v[192:195], v10 offset:11520
	ds_read_b128 v[196:199], v10 offset:11584
	s_waitcnt vmcnt(4)
	global_load_dwordx4 v[100:103], v8, s[48:49]
	global_load_dwordx4 v[104:107], v8, s[48:49] offset:64
	v_lshlrev_b32_e32 v234, 16, v92
	v_and_b32_e32 v235, 0xffff0000, v92
	v_pk_mul_f32 v[232:233], v[234:235], v[234:235]
	v_lshlrev_b32_e32 v234, 16, v93
	v_and_b32_e32 v235, 0xffff0000, v93
	v_pk_fma_f32 v[232:233], v[234:235], v[234:235], v[232:233]
	v_lshlrev_b32_e32 v234, 16, v94
	v_and_b32_e32 v235, 0xffff0000, v94
	v_pk_fma_f32 v[232:233], v[234:235], v[234:235], v[232:233]
	v_lshlrev_b32_e32 v234, 16, v95
	v_and_b32_e32 v235, 0xffff0000, v95
	v_pk_fma_f32 v[232:233], v[234:235], v[234:235], v[232:233]
	v_lshlrev_b32_e32 v234, 16, v96
	v_and_b32_e32 v235, 0xffff0000, v96
	v_pk_fma_f32 v[232:233], v[234:235], v[234:235], v[232:233]
	v_lshlrev_b32_e32 v234, 16, v97
	v_and_b32_e32 v235, 0xffff0000, v97
	v_pk_fma_f32 v[232:233], v[234:235], v[234:235], v[232:233]
	v_lshlrev_b32_e32 v234, 16, v98
	v_and_b32_e32 v235, 0xffff0000, v98
	v_pk_fma_f32 v[232:233], v[234:235], v[234:235], v[232:233]
	v_lshlrev_b32_e32 v234, 16, v99
	v_and_b32_e32 v235, 0xffff0000, v99
	v_pk_fma_f32 v[232:233], v[234:235], v[234:235], v[232:233]
	ds_read_b128 v[200:203], v10 offset:13824
	ds_read_b128 v[204:207], v10 offset:13888
	ds_read_b128 v[208:211], v10 offset:16128
	ds_read_b128 v[212:215], v10 offset:16192
	ds_read_b128 v[216:219], v10 offset:18432
	ds_read_b128 v[220:223], v10 offset:18496
	ds_read_b128 v[224:227], v10 offset:20736
	ds_read_b128 v[228:231], v10 offset:20800
	v_add_f32_e32 v232, v232, v233
	s_nop 0
	ds_bpermute_b32 v233, v15, v232
	s_waitcnt lgkmcnt(9)
	v_mfma_f32_16x16x32_bf16 v[108:111], v[160:163], v[92:95], 0
	v_mfma_f32_16x16x32_bf16 v[112:115], v[168:171], v[92:95], 0
	v_mfma_f32_16x16x32_bf16 v[116:119], v[176:179], v[92:95], 0
	v_mfma_f32_16x16x32_bf16 v[120:123], v[184:187], v[92:95], 0
	v_mfma_f32_16x16x32_bf16 v[124:127], v[192:195], v[92:95], 0
	v_mfma_f32_16x16x32_bf16 v[108:111], v[164:167], v[96:99], v[108:111]
	v_mfma_f32_16x16x32_bf16 v[112:115], v[172:175], v[96:99], v[112:115]
	v_mfma_f32_16x16x32_bf16 v[116:119], v[180:183], v[96:99], v[116:119]
	v_mfma_f32_16x16x32_bf16 v[120:123], v[188:191], v[96:99], v[120:123]
	v_mfma_f32_16x16x32_bf16 v[124:127], v[196:199], v[96:99], v[124:127]
	s_waitcnt lgkmcnt(0)
	v_add_f32_e32 v232, v232, v233
	v_mfma_f32_16x16x32_bf16 v[128:131], v[200:203], v[92:95], 0
	v_mfma_f32_16x16x32_bf16 v[132:135], v[208:211], v[92:95], 0
	v_mfma_f32_16x16x32_bf16 v[136:139], v[216:219], v[92:95], 0
	v_mfma_f32_16x16x32_bf16 v[140:143], v[224:227], v[92:95], 0
	ds_bpermute_b32 v233, v16, v232
	v_mfma_f32_16x16x32_bf16 v[128:131], v[204:207], v[96:99], v[128:131]
	v_mfma_f32_16x16x32_bf16 v[132:135], v[212:215], v[96:99], v[132:135]
	v_mfma_f32_16x16x32_bf16 v[136:139], v[220:223], v[96:99], v[136:139]
	v_mfma_f32_16x16x32_bf16 v[140:143], v[228:231], v[96:99], v[140:143]
	ds_read2_b64 v[160:163], v11 offset0:4 offset1:8
	ds_read2_b64 v[164:167], v12 offset0:4 offset1:8
	ds_read2_b64 v[168:171], v13 offset0:4 offset1:8
	ds_read2_b64 v[172:175], v14 offset0:4 offset1:8
	ds_read2_b64 v[176:179], v11 offset0:12 offset1:16
	ds_read2_b64 v[180:183], v12 offset0:12 offset1:16
	ds_read2_b64 v[184:187], v13 offset0:12 offset1:16
	ds_read2_b64 v[188:191], v14 offset0:12 offset1:16
	ds_read2_b64 v[192:195], v11 offset0:20 offset1:24
	ds_read2_b64 v[196:199], v12 offset0:20 offset1:24
	ds_read2_b64 v[200:203], v13 offset0:20 offset1:24
	ds_read2_b64 v[204:207], v14 offset0:20 offset1:24
	s_waitcnt lgkmcnt(12)
	v_add_f32_e32 v232, v232, v233
	v_mul_f32_e32 v232, 0x3c800000, v232
	v_add_f32_e32 v232, 0x358637bd, v232
	v_rsq_f32_e32 v236, v232
	s_nop 0
	v_mov_b32_e32 v237, v236
	s_nop 1
	v_pk_fma_f32 v[108:109], v[108:109], v[236:237], v[52:53]
	v_pk_fma_f32 v[110:111], v[110:111], v[236:237], v[54:55]
	v_pk_fma_f32 v[112:113], v[112:113], v[236:237], v[56:57]
	v_pk_fma_f32 v[114:115], v[114:115], v[236:237], v[58:59]
	v_pk_fma_f32 v[116:117], v[116:117], v[236:237], v[60:61]
	v_pk_fma_f32 v[118:119], v[118:119], v[236:237], v[62:63]
	v_pk_fma_f32 v[120:121], v[120:121], v[236:237], v[64:65]
	v_pk_fma_f32 v[122:123], v[122:123], v[236:237], v[66:67]
	v_pk_fma_f32 v[124:125], v[124:125], v[236:237], v[68:69]
	v_pk_fma_f32 v[126:127], v[126:127], v[236:237], v[70:71]
	v_pk_fma_f32 v[128:129], v[128:129], v[236:237], v[72:73]
	v_pk_fma_f32 v[130:131], v[130:131], v[236:237], v[74:75]
	v_pk_fma_f32 v[132:133], v[132:133], v[236:237], v[76:77]
	v_pk_fma_f32 v[134:135], v[134:135], v[236:237], v[78:79]
	v_pk_fma_f32 v[136:137], v[136:137], v[236:237], v[80:81]
	v_pk_fma_f32 v[138:139], v[138:139], v[236:237], v[82:83]
	v_pk_fma_f32 v[140:141], v[140:141], v[236:237], v[84:85]
	v_pk_fma_f32 v[142:143], v[142:143], v[236:237], v[86:87]
	v_exp_f32_e32 v108, v108
	v_exp_f32_e32 v109, v109
	v_exp_f32_e32 v110, v110
	v_exp_f32_e32 v111, v111
	v_exp_f32_e32 v112, v112
	v_exp_f32_e32 v113, v113
	v_exp_f32_e32 v114, v114
	v_exp_f32_e32 v115, v115
	v_exp_f32_e32 v116, v116
	v_exp_f32_e32 v117, v117
	v_exp_f32_e32 v118, v118
	v_exp_f32_e32 v119, v119
	v_exp_f32_e32 v120, v120
	v_exp_f32_e32 v121, v121
	v_exp_f32_e32 v122, v122
	v_exp_f32_e32 v123, v123
	v_exp_f32_e32 v124, v124
	v_exp_f32_e32 v125, v125
	v_exp_f32_e32 v126, v126
	v_exp_f32_e32 v127, v127
	v_exp_f32_e32 v128, v128
	v_exp_f32_e32 v129, v129
	v_exp_f32_e32 v130, v130
	v_exp_f32_e32 v131, v131
	v_exp_f32_e32 v132, v132
	v_exp_f32_e32 v133, v133
	v_exp_f32_e32 v134, v134
	v_exp_f32_e32 v135, v135
	v_exp_f32_e32 v136, v136
	v_exp_f32_e32 v137, v137
	v_exp_f32_e32 v138, v138
	v_exp_f32_e32 v139, v139
	v_exp_f32_e32 v140, v140
	v_exp_f32_e32 v141, v141
	v_exp_f32_e32 v142, v142
	v_exp_f32_e32 v143, v143
	s_cmp_lg_u32 s36, 0
	s_cbranch_scc1 .Lat_m1
	v_mov_b32_e32 v108, 0
	v_mov_b32_e32 v109, 0
	v_mov_b32_e32 v110, 0
	v_mov_b32_e32 v111, 0
	v_mov_b32_e32 v112, 0
	v_mov_b32_e32 v113, 0
	v_mov_b32_e32 v114, 0
	v_mov_b32_e32 v115, 0
	v_mov_b32_e32 v116, 0
	v_mov_b32_e32 v117, 0
	v_mov_b32_e32 v118, 0
	v_mov_b32_e32 v119, 0
	v_mov_b32_e32 v120, 0
	v_mov_b32_e32 v121, 0
	v_mov_b32_e32 v122, 0
	v_mov_b32_e32 v123, 0
	v_mov_b32_e32 v124, 0
	v_mov_b32_e32 v125, 0
	v_mov_b32_e32 v126, 0
	v_mov_b32_e32 v127, 0
	v_mov_b32_e32 v128, 0
	v_mov_b32_e32 v129, 0
	v_mov_b32_e32 v130, 0
	v_mov_b32_e32 v131, 0
	v_mov_b32_e32 v132, 0
	v_mov_b32_e32 v133, 0
	v_mov_b32_e32 v134, 0
	v_mov_b32_e32 v135, 0
.Lat_m1:
	s_nop 0
	v_pk_add_f32 v[232:233], v[108:109], v[110:111]
	v_pk_add_f32 v[234:235], v[112:113], v[114:115]
	v_pk_add_f32 v[232:233], v[232:233], v[116:117]
	v_pk_add_f32 v[234:235], v[234:235], v[118:119]
	v_pk_add_f32 v[232:233], v[232:233], v[120:121]
	v_pk_add_f32 v[234:235], v[234:235], v[122:123]
	v_pk_add_f32 v[232:233], v[232:233], v[124:125]
	v_pk_add_f32 v[234:235], v[234:235], v[126:127]
	v_pk_add_f32 v[232:233], v[232:233], v[128:129]
	v_pk_add_f32 v[234:235], v[234:235], v[130:131]
	v_pk_add_f32 v[232:233], v[232:233], v[132:133]
	v_pk_add_f32 v[234:235], v[234:235], v[134:135]
	v_pk_add_f32 v[232:233], v[232:233], v[136:137]
	v_pk_add_f32 v[234:235], v[234:235], v[138:139]
	v_pk_add_f32 v[232:233], v[232:233], v[140:141]
	v_pk_add_f32 v[234:235], v[234:235], v[142:143]
	v_pk_add_f32 v[232:233], v[232:233], v[234:235]
	s_nop 0
	v_add_f32_e32 v232, v232, v233
	v_cvt_pk_bf16_f32 v108, v108, v109
	v_cvt_pk_bf16_f32 v109, v110, v111
	v_cvt_pk_bf16_f32 v110, v112, v113
	v_cvt_pk_bf16_f32 v111, v114, v115
	v_cvt_pk_bf16_f32 v116, v116, v117
	v_cvt_pk_bf16_f32 v117, v118, v119
	v_cvt_pk_bf16_f32 v118, v120, v121
	v_cvt_pk_bf16_f32 v119, v122, v123
	v_cvt_pk_bf16_f32 v124, v124, v125
	v_cvt_pk_bf16_f32 v125, v126, v127
	v_cvt_pk_bf16_f32 v126, v128, v129
	v_cvt_pk_bf16_f32 v127, v130, v131
	v_cvt_pk_bf16_f32 v132, v132, v133
	v_cvt_pk_bf16_f32 v133, v134, v135
	v_cvt_pk_bf16_f32 v134, v136, v137
	v_cvt_pk_bf16_f32 v135, v138, v139
	v_cvt_pk_bf16_f32 v140, v140, v141
	v_cvt_pk_bf16_f32 v141, v142, v143
	v_mov_b32_e32 v142, 0
	v_mov_b32_e32 v143, 0
	ds_bpermute_b32 v233, v15, v232
	s_waitcnt lgkmcnt(1)
	v_mfma_f32_16x16x32_bf16 v[144:147], v[160:163], v[108:111], 0
	v_mfma_f32_16x16x32_bf16 v[148:151], v[164:167], v[108:111], 0
	v_mfma_f32_16x16x32_bf16 v[152:155], v[168:171], v[108:111], 0
	v_mfma_f32_16x16x32_bf16 v[156:159], v[172:175], v[108:111], 0
	v_mfma_f32_16x16x32_bf16 v[144:147], v[176:179], v[116:119], v[144:147]
	v_mfma_f32_16x16x32_bf16 v[148:151], v[180:183], v[116:119], v[148:151]
	v_mfma_f32_16x16x32_bf16 v[152:155], v[184:187], v[116:119], v[152:155]
	v_mfma_f32_16x16x32_bf16 v[156:159], v[188:191], v[116:119], v[156:159]
	v_mfma_f32_16x16x32_bf16 v[144:147], v[192:195], v[124:127], v[144:147]
	v_mfma_f32_16x16x32_bf16 v[148:151], v[196:199], v[124:127], v[148:151]
	v_mfma_f32_16x16x32_bf16 v[152:155], v[200:203], v[124:127], v[152:155]
	v_mfma_f32_16x16x32_bf16 v[156:159], v[204:207], v[124:127], v[156:159]
	ds_read2_b64 v[160:163], v11 offset0:28 offset1:32
	ds_read2_b64 v[164:167], v12 offset0:28 offset1:32
	ds_read2_b64 v[168:171], v13 offset0:28 offset1:32
	ds_read2_b64 v[172:175], v14 offset0:28 offset1:32
	ds_read2_b64 v[176:179], v11 offset0:36 offset1:36
	ds_read2_b64 v[180:183], v12 offset0:36 offset1:36
	ds_read2_b64 v[184:187], v13 offset0:36 offset1:36
	ds_read2_b64 v[188:191], v14 offset0:36 offset1:36
	s_waitcnt lgkmcnt(8)
	v_add_f32_e32 v232, v232, v233
	s_nop 0
	ds_bpermute_b32 v233, v16, v232
	s_waitcnt lgkmcnt(1)
	v_mfma_f32_16x16x32_bf16 v[144:147], v[160:163], v[132:135], v[144:147]
	v_mfma_f32_16x16x32_bf16 v[148:151], v[164:167], v[132:135], v[148:151]
	v_mfma_f32_16x16x32_bf16 v[152:155], v[168:171], v[132:135], v[152:155]
	v_mfma_f32_16x16x32_bf16 v[156:159], v[172:175], v[132:135], v[156:159]
	v_mfma_f32_16x16x32_bf16 v[144:147], v[176:179], v[140:143], v[144:147]
	v_mfma_f32_16x16x32_bf16 v[148:151], v[180:183], v[140:143], v[148:151]
	v_mfma_f32_16x16x32_bf16 v[152:155], v[184:187], v[140:143], v[152:155]
	v_mfma_f32_16x16x32_bf16 v[156:159], v[188:191], v[140:143], v[156:159]
	s_waitcnt lgkmcnt(0)
	v_add_f32_e32 v232, v232, v233
	v_add_f32_e32 v232, v232, v88
	v_rcp_f32_e32 v236, v232
	s_nop 0
	v_mov_b32_e32 v237, v236
	s_nop 4
	v_pk_mul_f32 v[144:145], v[144:145], v[236:237]
	v_pk_mul_f32 v[146:147], v[146:147], v[236:237]
	v_pk_mul_f32 v[148:149], v[148:149], v[236:237]
	v_pk_mul_f32 v[150:151], v[150:151], v[236:237]
	v_pk_mul_f32 v[152:153], v[152:153], v[236:237]
	v_pk_mul_f32 v[154:155], v[154:155], v[236:237]
	v_pk_mul_f32 v[156:157], v[156:157], v[236:237]
	v_pk_mul_f32 v[158:159], v[158:159], v[236:237]
	v_cvt_pk_bf16_f32 v144, v144, v145
	v_cvt_pk_bf16_f32 v145, v146, v147
	v_cvt_pk_bf16_f32 v148, v148, v149
	v_cvt_pk_bf16_f32 v149, v150, v151
	v_cvt_pk_bf16_f32 v152, v152, v153
	v_cvt_pk_bf16_f32 v153, v154, v155
	v_cvt_pk_bf16_f32 v156, v156, v157
	v_cvt_pk_bf16_f32 v157, v158, v159
	global_store_dwordx2 v9, v[144:145], s[50:51] offset:0
	global_store_dwordx2 v9, v[148:149], s[50:51] offset:32
	global_store_dwordx2 v9, v[152:153], s[50:51] offset:64
	global_store_dwordx2 v9, v[156:157], s[50:51] offset:96
	s_add_u32 s50, s50, 0x10000
	s_addc_u32 s51, s51, 0
	s_waitcnt vmcnt(4)
	v_mov_b32_e32 v92, v100
	v_mov_b32_e32 v93, v101
	v_mov_b32_e32 v94, v102
	v_mov_b32_e32 v95, v103
	v_mov_b32_e32 v96, v104
	v_mov_b32_e32 v97, v105
	v_mov_b32_e32 v98, v106
	v_mov_b32_e32 v99, v107
	s_add_u32 s48, s48, 0x14000
	s_addc_u32 s49, s49, 0
	ds_read_b128 v[160:163], v10 offset:4608
	ds_read_b128 v[164:167], v10 offset:4672
	ds_read_b128 v[168:171], v10 offset:6912
	ds_read_b128 v[172:175], v10 offset:6976
	ds_read_b128 v[176:179], v10 offset:9216
	ds_read_b128 v[180:183], v10 offset:9280
	ds_read_b128 v[184:187], v10 offset:11520
	ds_read_b128 v[188:191], v10 offset:11584
	ds_read_b128 v[192:195], v10 offset:13824
	ds_read_b128 v[196:199], v10 offset:13888
	s_waitcnt vmcnt(4)
	global_load_dwordx4 v[100:103], v8, s[48:49]
	global_load_dwordx4 v[104:107], v8, s[48:49] offset:64
	v_lshlrev_b32_e32 v234, 16, v92
	v_and_b32_e32 v235, 0xffff0000, v92
	v_pk_mul_f32 v[232:233], v[234:235], v[234:235]
	v_lshlrev_b32_e32 v234, 16, v93
	v_and_b32_e32 v235, 0xffff0000, v93
	v_pk_fma_f32 v[232:233], v[234:235], v[234:235], v[232:233]
	v_lshlrev_b32_e32 v234, 16, v94
	v_and_b32_e32 v235, 0xffff0000, v94
	v_pk_fma_f32 v[232:233], v[234:235], v[234:235], v[232:233]
	v_lshlrev_b32_e32 v234, 16, v95
	v_and_b32_e32 v235, 0xffff0000, v95
	v_pk_fma_f32 v[232:233], v[234:235], v[234:235], v[232:233]
	v_lshlrev_b32_e32 v234, 16, v96
	v_and_b32_e32 v235, 0xffff0000, v96
	v_pk_fma_f32 v[232:233], v[234:235], v[234:235], v[232:233]
	v_lshlrev_b32_e32 v234, 16, v97
	v_and_b32_e32 v235, 0xffff0000, v97
	v_pk_fma_f32 v[232:233], v[234:235], v[234:235], v[232:233]
	v_lshlrev_b32_e32 v234, 16, v98
	v_and_b32_e32 v235, 0xffff0000, v98
	v_pk_fma_f32 v[232:233], v[234:235], v[234:235], v[232:233]
	v_lshlrev_b32_e32 v234, 16, v99
	v_and_b32_e32 v235, 0xffff0000, v99
	v_pk_fma_f32 v[232:233], v[234:235], v[234:235], v[232:233]
	ds_read_b128 v[200:203], v10 offset:16128
	ds_read_b128 v[204:207], v10 offset:16192
	ds_read_b128 v[208:211], v10 offset:18432
	ds_read_b128 v[212:215], v10 offset:18496
	ds_read_b128 v[216:219], v10 offset:20736
	ds_read_b128 v[220:223], v10 offset:20800
	ds_read_b128 v[224:227], v10 offset:23040
	ds_read_b128 v[228:231], v10 offset:23104
	v_add_f32_e32 v232, v232, v233
	s_nop 0
	ds_bpermute_b32 v233, v15, v232
	s_waitcnt lgkmcnt(9)
	v_mfma_f32_16x16x32_bf16 v[108:111], v[160:163], v[92:95], 0
	v_mfma_f32_16x16x32_bf16 v[112:115], v[168:171], v[92:95], 0
	v_mfma_f32_16x16x32_bf16 v[116:119], v[176:179], v[92:95], 0
	v_mfma_f32_16x16x32_bf16 v[120:123], v[184:187], v[92:95], 0
	v_mfma_f32_16x16x32_bf16 v[124:127], v[192:195], v[92:95], 0
	v_mfma_f32_16x16x32_bf16 v[108:111], v[164:167], v[96:99], v[108:111]
	v_mfma_f32_16x16x32_bf16 v[112:115], v[172:175], v[96:99], v[112:115]
	v_mfma_f32_16x16x32_bf16 v[116:119], v[180:183], v[96:99], v[116:119]
	v_mfma_f32_16x16x32_bf16 v[120:123], v[188:191], v[96:99], v[120:123]
	v_mfma_f32_16x16x32_bf16 v[124:127], v[196:199], v[96:99], v[124:127]
	s_waitcnt lgkmcnt(0)
	v_add_f32_e32 v232, v232, v233
	v_mfma_f32_16x16x32_bf16 v[128:131], v[200:203], v[92:95], 0
	v_mfma_f32_16x16x32_bf16 v[132:135], v[208:211], v[92:95], 0
	v_mfma_f32_16x16x32_bf16 v[136:139], v[216:219], v[92:95], 0
	v_mfma_f32_16x16x32_bf16 v[140:143], v[224:227], v[92:95], 0
	ds_bpermute_b32 v233, v16, v232
	v_mfma_f32_16x16x32_bf16 v[128:131], v[204:207], v[96:99], v[128:131]
	v_mfma_f32_16x16x32_bf16 v[132:135], v[212:215], v[96:99], v[132:135]
	v_mfma_f32_16x16x32_bf16 v[136:139], v[220:223], v[96:99], v[136:139]
	v_mfma_f32_16x16x32_bf16 v[140:143], v[228:231], v[96:99], v[140:143]
	ds_read2_b64 v[160:163], v11 offset0:8 offset1:12
	ds_read2_b64 v[164:167], v12 offset0:8 offset1:12
	ds_read2_b64 v[168:171], v13 offset0:8 offset1:12
	ds_read2_b64 v[172:175], v14 offset0:8 offset1:12
	ds_read2_b64 v[176:179], v11 offset0:16 offset1:20
	ds_read2_b64 v[180:183], v12 offset0:16 offset1:20
	ds_read2_b64 v[184:187], v13 offset0:16 offset1:20
	ds_read2_b64 v[188:191], v14 offset0:16 offset1:20
	ds_read2_b64 v[192:195], v11 offset0:24 offset1:28
	ds_read2_b64 v[196:199], v12 offset0:24 offset1:28
	ds_read2_b64 v[200:203], v13 offset0:24 offset1:28
	ds_read2_b64 v[204:207], v14 offset0:24 offset1:28
	s_waitcnt lgkmcnt(12)
	v_add_f32_e32 v232, v232, v233
	v_mul_f32_e32 v232, 0x3c800000, v232
	v_add_f32_e32 v232, 0x358637bd, v232
	v_rsq_f32_e32 v236, v232
	s_nop 0
	v_mov_b32_e32 v237, v236
	s_nop 1
	v_pk_fma_f32 v[108:109], v[108:109], v[236:237], v[52:53]
	v_pk_fma_f32 v[110:111], v[110:111], v[236:237], v[54:55]
	v_pk_fma_f32 v[112:113], v[112:113], v[236:237], v[56:57]
	v_pk_fma_f32 v[114:115], v[114:115], v[236:237], v[58:59]
	v_pk_fma_f32 v[116:117], v[116:117], v[236:237], v[60:61]
	v_pk_fma_f32 v[118:119], v[118:119], v[236:237], v[62:63]
	v_pk_fma_f32 v[120:121], v[120:121], v[236:237], v[64:65]
	v_pk_fma_f32 v[122:123], v[122:123], v[236:237], v[66:67]
	v_pk_fma_f32 v[124:125], v[124:125], v[236:237], v[68:69]
	v_pk_fma_f32 v[126:127], v[126:127], v[236:237], v[70:71]
	v_pk_fma_f32 v[128:129], v[128:129], v[236:237], v[72:73]
	v_pk_fma_f32 v[130:131], v[130:131], v[236:237], v[74:75]
	v_pk_fma_f32 v[132:133], v[132:133], v[236:237], v[76:77]
	v_pk_fma_f32 v[134:135], v[134:135], v[236:237], v[78:79]
	v_pk_fma_f32 v[136:137], v[136:137], v[236:237], v[80:81]
	v_pk_fma_f32 v[138:139], v[138:139], v[236:237], v[82:83]
	v_pk_fma_f32 v[140:141], v[140:141], v[236:237], v[84:85]
	v_pk_fma_f32 v[142:143], v[142:143], v[236:237], v[86:87]
	v_exp_f32_e32 v108, v108
	v_exp_f32_e32 v109, v109
	v_exp_f32_e32 v110, v110
	v_exp_f32_e32 v111, v111
	v_exp_f32_e32 v112, v112
	v_exp_f32_e32 v113, v113
	v_exp_f32_e32 v114, v114
	v_exp_f32_e32 v115, v115
	v_exp_f32_e32 v116, v116
	v_exp_f32_e32 v117, v117
	v_exp_f32_e32 v118, v118
	v_exp_f32_e32 v119, v119
	v_exp_f32_e32 v120, v120
	v_exp_f32_e32 v121, v121
	v_exp_f32_e32 v122, v122
	v_exp_f32_e32 v123, v123
	v_exp_f32_e32 v124, v124
	v_exp_f32_e32 v125, v125
	v_exp_f32_e32 v126, v126
	v_exp_f32_e32 v127, v127
	v_exp_f32_e32 v128, v128
	v_exp_f32_e32 v129, v129
	v_exp_f32_e32 v130, v130
	v_exp_f32_e32 v131, v131
	v_exp_f32_e32 v132, v132
	v_exp_f32_e32 v133, v133
	v_exp_f32_e32 v134, v134
	v_exp_f32_e32 v135, v135
	v_exp_f32_e32 v136, v136
	v_exp_f32_e32 v137, v137
	v_exp_f32_e32 v138, v138
	v_exp_f32_e32 v139, v139
	v_exp_f32_e32 v140, v140
	v_exp_f32_e32 v141, v141
	v_exp_f32_e32 v142, v142
	v_exp_f32_e32 v143, v143
	s_cmp_lg_u32 s36, 0
	s_cbranch_scc1 .Lat_m2
	v_mov_b32_e32 v108, 0
	v_mov_b32_e32 v109, 0
	v_mov_b32_e32 v110, 0
	v_mov_b32_e32 v111, 0
	v_mov_b32_e32 v112, 0
	v_mov_b32_e32 v113, 0
	v_mov_b32_e32 v114, 0
	v_mov_b32_e32 v115, 0
	v_mov_b32_e32 v116, 0
	v_mov_b32_e32 v117, 0
	v_mov_b32_e32 v118, 0
	v_mov_b32_e32 v119, 0
	v_mov_b32_e32 v120, 0
	v_mov_b32_e32 v121, 0
	v_mov_b32_e32 v122, 0
	v_mov_b32_e32 v123, 0
	v_mov_b32_e32 v124, 0
	v_mov_b32_e32 v125, 0
	v_mov_b32_e32 v126, 0
	v_mov_b32_e32 v127, 0
	v_mov_b32_e32 v128, 0
	v_mov_b32_e32 v129, 0
	v_mov_b32_e32 v130, 0
	v_mov_b32_e32 v131, 0
.Lat_m2:
	s_nop 0
	v_pk_add_f32 v[232:233], v[108:109], v[110:111]
	v_pk_add_f32 v[234:235], v[112:113], v[114:115]
	v_pk_add_f32 v[232:233], v[232:233], v[116:117]
	v_pk_add_f32 v[234:235], v[234:235], v[118:119]
	v_pk_add_f32 v[232:233], v[232:233], v[120:121]
	v_pk_add_f32 v[234:235], v[234:235], v[122:123]
	v_pk_add_f32 v[232:233], v[232:233], v[124:125]
	v_pk_add_f32 v[234:235], v[234:235], v[126:127]
	v_pk_add_f32 v[232:233], v[232:233], v[128:129]
	v_pk_add_f32 v[234:235], v[234:235], v[130:131]
	v_pk_add_f32 v[232:233], v[232:233], v[132:133]
	v_pk_add_f32 v[234:235], v[234:235], v[134:135]
	v_pk_add_f32 v[232:233], v[232:233], v[136:137]
	v_pk_add_f32 v[234:235], v[234:235], v[138:139]
	v_pk_add_f32 v[232:233], v[232:233], v[140:141]
	v_pk_add_f32 v[234:235], v[234:235], v[142:143]
	v_pk_add_f32 v[232:233], v[232:233], v[234:235]
	s_nop 0
	v_add_f32_e32 v232, v232, v233
	v_cvt_pk_bf16_f32 v108, v108, v109
	v_cvt_pk_bf16_f32 v109, v110, v111
	v_cvt_pk_bf16_f32 v110, v112, v113
	v_cvt_pk_bf16_f32 v111, v114, v115
	v_cvt_pk_bf16_f32 v116, v116, v117
	v_cvt_pk_bf16_f32 v117, v118, v119
	v_cvt_pk_bf16_f32 v118, v120, v121
	v_cvt_pk_bf16_f32 v119, v122, v123
	v_cvt_pk_bf16_f32 v124, v124, v125
	v_cvt_pk_bf16_f32 v125, v126, v127
	v_cvt_pk_bf16_f32 v126, v128, v129
	v_cvt_pk_bf16_f32 v127, v130, v131
	v_cvt_pk_bf16_f32 v132, v132, v133
	v_cvt_pk_bf16_f32 v133, v134, v135
	v_cvt_pk_bf16_f32 v134, v136, v137
	v_cvt_pk_bf16_f32 v135, v138, v139
	v_cvt_pk_bf16_f32 v140, v140, v141
	v_cvt_pk_bf16_f32 v141, v142, v143
	v_mov_b32_e32 v142, 0
	v_mov_b32_e32 v143, 0
	ds_bpermute_b32 v233, v15, v232
	s_waitcnt lgkmcnt(1)
	v_mfma_f32_16x16x32_bf16 v[144:147], v[160:163], v[108:111], 0
	v_mfma_f32_16x16x32_bf16 v[148:151], v[164:167], v[108:111], 0
	v_mfma_f32_16x16x32_bf16 v[152:155], v[168:171], v[108:111], 0
	v_mfma_f32_16x16x32_bf16 v[156:159], v[172:175], v[108:111], 0
	v_mfma_f32_16x16x32_bf16 v[144:147], v[176:179], v[116:119], v[144:147]
	v_mfma_f32_16x16x32_bf16 v[148:151], v[180:183], v[116:119], v[148:151]
	v_mfma_f32_16x16x32_bf16 v[152:155], v[184:187], v[116:119], v[152:155]
	v_mfma_f32_16x16x32_bf16 v[156:159], v[188:191], v[116:119], v[156:159]
	v_mfma_f32_16x16x32_bf16 v[144:147], v[192:195], v[124:127], v[144:147]
	v_mfma_f32_16x16x32_bf16 v[148:151], v[196:199], v[124:127], v[148:151]
	v_mfma_f32_16x16x32_bf16 v[152:155], v[200:203], v[124:127], v[152:155]
	v_mfma_f32_16x16x32_bf16 v[156:159], v[204:207], v[124:127], v[156:159]
	ds_read2_b64 v[160:163], v11 offset0:32 offset1:36
	ds_read2_b64 v[164:167], v12 offset0:32 offset1:36
	ds_read2_b64 v[168:171], v13 offset0:32 offset1:36
	ds_read2_b64 v[172:175], v14 offset0:32 offset1:36
	ds_read2_b64 v[176:179], v11 offset0:40 offset1:40
	ds_read2_b64 v[180:183], v12 offset0:40 offset1:40
	ds_read2_b64 v[184:187], v13 offset0:40 offset1:40
	ds_read2_b64 v[188:191], v14 offset0:40 offset1:40
	s_waitcnt lgkmcnt(8)
	v_add_f32_e32 v232, v232, v233
	s_nop 0
	ds_bpermute_b32 v233, v16, v232
	s_waitcnt lgkmcnt(1)
	v_mfma_f32_16x16x32_bf16 v[144:147], v[160:163], v[132:135], v[144:147]
	v_mfma_f32_16x16x32_bf16 v[148:151], v[164:167], v[132:135], v[148:151]
	v_mfma_f32_16x16x32_bf16 v[152:155], v[168:171], v[132:135], v[152:155]
	v_mfma_f32_16x16x32_bf16 v[156:159], v[172:175], v[132:135], v[156:159]
	v_mfma_f32_16x16x32_bf16 v[144:147], v[176:179], v[140:143], v[144:147]
	v_mfma_f32_16x16x32_bf16 v[148:151], v[180:183], v[140:143], v[148:151]
	v_mfma_f32_16x16x32_bf16 v[152:155], v[184:187], v[140:143], v[152:155]
	v_mfma_f32_16x16x32_bf16 v[156:159], v[188:191], v[140:143], v[156:159]
	s_waitcnt lgkmcnt(0)
	v_add_f32_e32 v232, v232, v233
	v_add_f32_e32 v232, v232, v88
	v_rcp_f32_e32 v236, v232
	s_nop 0
	v_mov_b32_e32 v237, v236
	s_nop 4
	v_pk_mul_f32 v[144:145], v[144:145], v[236:237]
	v_pk_mul_f32 v[146:147], v[146:147], v[236:237]
	v_pk_mul_f32 v[148:149], v[148:149], v[236:237]
	v_pk_mul_f32 v[150:151], v[150:151], v[236:237]
	v_pk_mul_f32 v[152:153], v[152:153], v[236:237]
	v_pk_mul_f32 v[154:155], v[154:155], v[236:237]
	v_pk_mul_f32 v[156:157], v[156:157], v[236:237]
	v_pk_mul_f32 v[158:159], v[158:159], v[236:237]
	v_cvt_pk_bf16_f32 v144, v144, v145
	v_cvt_pk_bf16_f32 v145, v146, v147
	v_cvt_pk_bf16_f32 v148, v148, v149
	v_cvt_pk_bf16_f32 v149, v150, v151
	v_cvt_pk_bf16_f32 v152, v152, v153
	v_cvt_pk_bf16_f32 v153, v154, v155
	v_cvt_pk_bf16_f32 v156, v156, v157
	v_cvt_pk_bf16_f32 v157, v158, v159
	global_store_dwordx2 v9, v[144:145], s[50:51] offset:0
	global_store_dwordx2 v9, v[148:149], s[50:51] offset:32
	global_store_dwordx2 v9, v[152:153], s[50:51] offset:64
	global_store_dwordx2 v9, v[156:157], s[50:51] offset:96
	s_add_u32 s50, s50, 0x10000
	s_addc_u32 s51, s51, 0
	s_waitcnt vmcnt(4)
	v_mov_b32_e32 v92, v100
	v_mov_b32_e32 v93, v101
	v_mov_b32_e32 v94, v102
	v_mov_b32_e32 v95, v103
	v_mov_b32_e32 v96, v104
	v_mov_b32_e32 v97, v105
	v_mov_b32_e32 v98, v106
	v_mov_b32_e32 v99, v107
	s_add_u32 s48, s48, 0x14000
	s_addc_u32 s49, s49, 0
	ds_read_b128 v[160:163], v10 offset:6912
	ds_read_b128 v[164:167], v10 offset:6976
	ds_read_b128 v[168:171], v10 offset:9216
	ds_read_b128 v[172:175], v10 offset:9280
	ds_read_b128 v[176:179], v10 offset:11520
	ds_read_b128 v[180:183], v10 offset:11584
	ds_read_b128 v[184:187], v10 offset:13824
	ds_read_b128 v[188:191], v10 offset:13888
	ds_read_b128 v[192:195], v10 offset:16128
	ds_read_b128 v[196:199], v10 offset:16192
	s_waitcnt vmcnt(4)
	global_load_dwordx4 v[100:103], v8, s[48:49]
	global_load_dwordx4 v[104:107], v8, s[48:49] offset:64
	v_lshlrev_b32_e32 v234, 16, v92
	v_and_b32_e32 v235, 0xffff0000, v92
	v_pk_mul_f32 v[232:233], v[234:235], v[234:235]
	v_lshlrev_b32_e32 v234, 16, v93
	v_and_b32_e32 v235, 0xffff0000, v93
	v_pk_fma_f32 v[232:233], v[234:235], v[234:235], v[232:233]
	v_lshlrev_b32_e32 v234, 16, v94
	v_and_b32_e32 v235, 0xffff0000, v94
	v_pk_fma_f32 v[232:233], v[234:235], v[234:235], v[232:233]
	v_lshlrev_b32_e32 v234, 16, v95
	v_and_b32_e32 v235, 0xffff0000, v95
	v_pk_fma_f32 v[232:233], v[234:235], v[234:235], v[232:233]
	v_lshlrev_b32_e32 v234, 16, v96
	v_and_b32_e32 v235, 0xffff0000, v96
	v_pk_fma_f32 v[232:233], v[234:235], v[234:235], v[232:233]
	v_lshlrev_b32_e32 v234, 16, v97
	v_and_b32_e32 v235, 0xffff0000, v97
	v_pk_fma_f32 v[232:233], v[234:235], v[234:235], v[232:233]
	v_lshlrev_b32_e32 v234, 16, v98
	v_and_b32_e32 v235, 0xffff0000, v98
	v_pk_fma_f32 v[232:233], v[234:235], v[234:235], v[232:233]
	v_lshlrev_b32_e32 v234, 16, v99
	v_and_b32_e32 v235, 0xffff0000, v99
	v_pk_fma_f32 v[232:233], v[234:235], v[234:235], v[232:233]
	ds_read_b128 v[200:203], v10 offset:18432
	ds_read_b128 v[204:207], v10 offset:18496
	ds_read_b128 v[208:211], v10 offset:20736
	ds_read_b128 v[212:215], v10 offset:20800
	ds_read_b128 v[216:219], v10 offset:23040
	ds_read_b128 v[220:223], v10 offset:23104
	ds_read_b128 v[224:227], v10 offset:25344
	ds_read_b128 v[228:231], v10 offset:25408
	v_add_f32_e32 v232, v232, v233
	s_nop 0
	ds_bpermute_b32 v233, v15, v232
	s_waitcnt lgkmcnt(9)
	v_mfma_f32_16x16x32_bf16 v[108:111], v[160:163], v[92:95], 0
	v_mfma_f32_16x16x32_bf16 v[112:115], v[168:171], v[92:95], 0
	v_mfma_f32_16x16x32_bf16 v[116:119], v[176:179], v[92:95], 0
	v_mfma_f32_16x16x32_bf16 v[120:123], v[184:187], v[92:95], 0
	v_mfma_f32_16x16x32_bf16 v[124:127], v[192:195], v[92:95], 0
	v_mfma_f32_16x16x32_bf16 v[108:111], v[164:167], v[96:99], v[108:111]
	v_mfma_f32_16x16x32_bf16 v[112:115], v[172:175], v[96:99], v[112:115]
	v_mfma_f32_16x16x32_bf16 v[116:119], v[180:183], v[96:99], v[116:119]
	v_mfma_f32_16x16x32_bf16 v[120:123], v[188:191], v[96:99], v[120:123]
	v_mfma_f32_16x16x32_bf16 v[124:127], v[196:199], v[96:99], v[124:127]
	s_waitcnt lgkmcnt(0)
	v_add_f32_e32 v232, v232, v233
	v_mfma_f32_16x16x32_bf16 v[128:131], v[200:203], v[92:95], 0
	v_mfma_f32_16x16x32_bf16 v[132:135], v[208:211], v[92:95], 0
	v_mfma_f32_16x16x32_bf16 v[136:139], v[216:219], v[92:95], 0
	v_mfma_f32_16x16x32_bf16 v[140:143], v[224:227], v[92:95], 0
	ds_bpermute_b32 v233, v16, v232
	v_mfma_f32_16x16x32_bf16 v[128:131], v[204:207], v[96:99], v[128:131]
	v_mfma_f32_16x16x32_bf16 v[132:135], v[212:215], v[96:99], v[132:135]
	v_mfma_f32_16x16x32_bf16 v[136:139], v[220:223], v[96:99], v[136:139]
	v_mfma_f32_16x16x32_bf16 v[140:143], v[228:231], v[96:99], v[140:143]
	ds_read2_b64 v[160:163], v11 offset0:12 offset1:16
	ds_read2_b64 v[164:167], v12 offset0:12 offset1:16
	ds_read2_b64 v[168:171], v13 offset0:12 offset1:16
	ds_read2_b64 v[172:175], v14 offset0:12 offset1:16
	ds_read2_b64 v[176:179], v11 offset0:20 offset1:24
	ds_read2_b64 v[180:183], v12 offset0:20 offset1:24
	ds_read2_b64 v[184:187], v13 offset0:20 offset1:24
	ds_read2_b64 v[188:191], v14 offset0:20 offset1:24
	ds_read2_b64 v[192:195], v11 offset0:28 offset1:32
	ds_read2_b64 v[196:199], v12 offset0:28 offset1:32
	ds_read2_b64 v[200:203], v13 offset0:28 offset1:32
	ds_read2_b64 v[204:207], v14 offset0:28 offset1:32
	s_waitcnt lgkmcnt(12)
	v_add_f32_e32 v232, v232, v233
	v_mul_f32_e32 v232, 0x3c800000, v232
	v_add_f32_e32 v232, 0x358637bd, v232
	v_rsq_f32_e32 v236, v232
	s_nop 0
	v_mov_b32_e32 v237, v236
	s_nop 1
	v_pk_fma_f32 v[108:109], v[108:109], v[236:237], v[52:53]
	v_pk_fma_f32 v[110:111], v[110:111], v[236:237], v[54:55]
	v_pk_fma_f32 v[112:113], v[112:113], v[236:237], v[56:57]
	v_pk_fma_f32 v[114:115], v[114:115], v[236:237], v[58:59]
	v_pk_fma_f32 v[116:117], v[116:117], v[236:237], v[60:61]
	v_pk_fma_f32 v[118:119], v[118:119], v[236:237], v[62:63]
	v_pk_fma_f32 v[120:121], v[120:121], v[236:237], v[64:65]
	v_pk_fma_f32 v[122:123], v[122:123], v[236:237], v[66:67]
	v_pk_fma_f32 v[124:125], v[124:125], v[236:237], v[68:69]
	v_pk_fma_f32 v[126:127], v[126:127], v[236:237], v[70:71]
	v_pk_fma_f32 v[128:129], v[128:129], v[236:237], v[72:73]
	v_pk_fma_f32 v[130:131], v[130:131], v[236:237], v[74:75]
	v_pk_fma_f32 v[132:133], v[132:133], v[236:237], v[76:77]
	v_pk_fma_f32 v[134:135], v[134:135], v[236:237], v[78:79]
	v_pk_fma_f32 v[136:137], v[136:137], v[236:237], v[80:81]
	v_pk_fma_f32 v[138:139], v[138:139], v[236:237], v[82:83]
	v_pk_fma_f32 v[140:141], v[140:141], v[236:237], v[84:85]
	v_pk_fma_f32 v[142:143], v[142:143], v[236:237], v[86:87]
	v_exp_f32_e32 v108, v108
	v_exp_f32_e32 v109, v109
	v_exp_f32_e32 v110, v110
	v_exp_f32_e32 v111, v111
	v_exp_f32_e32 v112, v112
	v_exp_f32_e32 v113, v113
	v_exp_f32_e32 v114, v114
	v_exp_f32_e32 v115, v115
	v_exp_f32_e32 v116, v116
	v_exp_f32_e32 v117, v117
	v_exp_f32_e32 v118, v118
	v_exp_f32_e32 v119, v119
	v_exp_f32_e32 v120, v120
	v_exp_f32_e32 v121, v121
	v_exp_f32_e32 v122, v122
	v_exp_f32_e32 v123, v123
	v_exp_f32_e32 v124, v124
	v_exp_f32_e32 v125, v125
	v_exp_f32_e32 v126, v126
	v_exp_f32_e32 v127, v127
	v_exp_f32_e32 v128, v128
	v_exp_f32_e32 v129, v129
	v_exp_f32_e32 v130, v130
	v_exp_f32_e32 v131, v131
	v_exp_f32_e32 v132, v132
	v_exp_f32_e32 v133, v133
	v_exp_f32_e32 v134, v134
	v_exp_f32_e32 v135, v135
	v_exp_f32_e32 v136, v136
	v_exp_f32_e32 v137, v137
	v_exp_f32_e32 v138, v138
	v_exp_f32_e32 v139, v139
	v_exp_f32_e32 v140, v140
	v_exp_f32_e32 v141, v141
	v_exp_f32_e32 v142, v142
	v_exp_f32_e32 v143, v143
	s_cmp_lg_u32 s36, 0
	s_cbranch_scc1 .Lat_m3
	v_mov_b32_e32 v108, 0
	v_mov_b32_e32 v109, 0
	v_mov_b32_e32 v110, 0
	v_mov_b32_e32 v111, 0
	v_mov_b32_e32 v112, 0
	v_mov_b32_e32 v113, 0
	v_mov_b32_e32 v114, 0
	v_mov_b32_e32 v115, 0
	v_mov_b32_e32 v116, 0
	v_mov_b32_e32 v117, 0
	v_mov_b32_e32 v118, 0
	v_mov_b32_e32 v119, 0
	v_mov_b32_e32 v120, 0
	v_mov_b32_e32 v121, 0
	v_mov_b32_e32 v122, 0
	v_mov_b32_e32 v123, 0
	v_mov_b32_e32 v124, 0
	v_mov_b32_e32 v125, 0
	v_mov_b32_e32 v126, 0
	v_mov_b32_e32 v127, 0
.Lat_m3:
	s_nop 0
	v_pk_add_f32 v[232:233], v[108:109], v[110:111]
	v_pk_add_f32 v[234:235], v[112:113], v[114:115]
	v_pk_add_f32 v[232:233], v[232:233], v[116:117]
	v_pk_add_f32 v[234:235], v[234:235], v[118:119]
	v_pk_add_f32 v[232:233], v[232:233], v[120:121]
	v_pk_add_f32 v[234:235], v[234:235], v[122:123]
	v_pk_add_f32 v[232:233], v[232:233], v[124:125]
	v_pk_add_f32 v[234:235], v[234:235], v[126:127]
	v_pk_add_f32 v[232:233], v[232:233], v[128:129]
	v_pk_add_f32 v[234:235], v[234:235], v[130:131]
	v_pk_add_f32 v[232:233], v[232:233], v[132:133]
	v_pk_add_f32 v[234:235], v[234:235], v[134:135]
	v_pk_add_f32 v[232:233], v[232:233], v[136:137]
	v_pk_add_f32 v[234:235], v[234:235], v[138:139]
	v_pk_add_f32 v[232:233], v[232:233], v[140:141]
	v_pk_add_f32 v[234:235], v[234:235], v[142:143]
	v_pk_add_f32 v[232:233], v[232:233], v[234:235]
	s_nop 0
	v_add_f32_e32 v232, v232, v233
	v_cvt_pk_bf16_f32 v108, v108, v109
	v_cvt_pk_bf16_f32 v109, v110, v111
	v_cvt_pk_bf16_f32 v110, v112, v113
	v_cvt_pk_bf16_f32 v111, v114, v115
	v_cvt_pk_bf16_f32 v116, v116, v117
	v_cvt_pk_bf16_f32 v117, v118, v119
	v_cvt_pk_bf16_f32 v118, v120, v121
	v_cvt_pk_bf16_f32 v119, v122, v123
	v_cvt_pk_bf16_f32 v124, v124, v125
	v_cvt_pk_bf16_f32 v125, v126, v127
	v_cvt_pk_bf16_f32 v126, v128, v129
	v_cvt_pk_bf16_f32 v127, v130, v131
	v_cvt_pk_bf16_f32 v132, v132, v133
	v_cvt_pk_bf16_f32 v133, v134, v135
	v_cvt_pk_bf16_f32 v134, v136, v137
	v_cvt_pk_bf16_f32 v135, v138, v139
	v_cvt_pk_bf16_f32 v140, v140, v141
	v_cvt_pk_bf16_f32 v141, v142, v143
	v_mov_b32_e32 v142, 0
	v_mov_b32_e32 v143, 0
	ds_bpermute_b32 v233, v15, v232
	s_waitcnt lgkmcnt(1)
	v_mfma_f32_16x16x32_bf16 v[144:147], v[160:163], v[108:111], 0
	v_mfma_f32_16x16x32_bf16 v[148:151], v[164:167], v[108:111], 0
	v_mfma_f32_16x16x32_bf16 v[152:155], v[168:171], v[108:111], 0
	v_mfma_f32_16x16x32_bf16 v[156:159], v[172:175], v[108:111], 0
	v_mfma_f32_16x16x32_bf16 v[144:147], v[176:179], v[116:119], v[144:147]
	v_mfma_f32_16x16x32_bf16 v[148:151], v[180:183], v[116:119], v[148:151]
	v_mfma_f32_16x16x32_bf16 v[152:155], v[184:187], v[116:119], v[152:155]
	v_mfma_f32_16x16x32_bf16 v[156:159], v[188:191], v[116:119], v[156:159]
	v_mfma_f32_16x16x32_bf16 v[144:147], v[192:195], v[124:127], v[144:147]
	v_mfma_f32_16x16x32_bf16 v[148:151], v[196:199], v[124:127], v[148:151]
	v_mfma_f32_16x16x32_bf16 v[152:155], v[200:203], v[124:127], v[152:155]
	v_mfma_f32_16x16x32_bf16 v[156:159], v[204:207], v[124:127], v[156:159]
	ds_read2_b64 v[160:163], v11 offset0:36 offset1:40
	ds_read2_b64 v[164:167], v12 offset0:36 offset1:40
	ds_read2_b64 v[168:171], v13 offset0:36 offset1:40
	ds_read2_b64 v[172:175], v14 offset0:36 offset1:40
	ds_read2_b64 v[176:179], v11 offset0:44 offset1:44
	ds_read2_b64 v[180:183], v12 offset0:44 offset1:44
	ds_read2_b64 v[184:187], v13 offset0:44 offset1:44
	ds_read2_b64 v[188:191], v14 offset0:44 offset1:44
	s_waitcnt lgkmcnt(8)
	v_add_f32_e32 v232, v232, v233
	s_nop 0
	ds_bpermute_b32 v233, v16, v232
	s_waitcnt lgkmcnt(1)
	v_mfma_f32_16x16x32_bf16 v[144:147], v[160:163], v[132:135], v[144:147]
	v_mfma_f32_16x16x32_bf16 v[148:151], v[164:167], v[132:135], v[148:151]
	v_mfma_f32_16x16x32_bf16 v[152:155], v[168:171], v[132:135], v[152:155]
	v_mfma_f32_16x16x32_bf16 v[156:159], v[172:175], v[132:135], v[156:159]
	v_mfma_f32_16x16x32_bf16 v[144:147], v[176:179], v[140:143], v[144:147]
	v_mfma_f32_16x16x32_bf16 v[148:151], v[180:183], v[140:143], v[148:151]
	v_mfma_f32_16x16x32_bf16 v[152:155], v[184:187], v[140:143], v[152:155]
	v_mfma_f32_16x16x32_bf16 v[156:159], v[188:191], v[140:143], v[156:159]
	s_waitcnt lgkmcnt(0)
	v_add_f32_e32 v232, v232, v233
	v_add_f32_e32 v232, v232, v88
	v_rcp_f32_e32 v236, v232
	s_nop 0
	v_mov_b32_e32 v237, v236
	s_nop 4
	v_pk_mul_f32 v[144:145], v[144:145], v[236:237]
	v_pk_mul_f32 v[146:147], v[146:147], v[236:237]
	v_pk_mul_f32 v[148:149], v[148:149], v[236:237]
	v_pk_mul_f32 v[150:151], v[150:151], v[236:237]
	v_pk_mul_f32 v[152:153], v[152:153], v[236:237]
	v_pk_mul_f32 v[154:155], v[154:155], v[236:237]
	v_pk_mul_f32 v[156:157], v[156:157], v[236:237]
	v_pk_mul_f32 v[158:159], v[158:159], v[236:237]
	v_cvt_pk_bf16_f32 v144, v144, v145
	v_cvt_pk_bf16_f32 v145, v146, v147
	v_cvt_pk_bf16_f32 v148, v148, v149
	v_cvt_pk_bf16_f32 v149, v150, v151
	v_cvt_pk_bf16_f32 v152, v152, v153
	v_cvt_pk_bf16_f32 v153, v154, v155
	v_cvt_pk_bf16_f32 v156, v156, v157
	v_cvt_pk_bf16_f32 v157, v158, v159
	global_store_dwordx2 v9, v[144:145], s[50:51] offset:0
	global_store_dwordx2 v9, v[148:149], s[50:51] offset:32
	global_store_dwordx2 v9, v[152:153], s[50:51] offset:64
	global_store_dwordx2 v9, v[156:157], s[50:51] offset:96
	s_add_u32 s50, s50, 0x10000
	s_addc_u32 s51, s51, 0
	s_waitcnt vmcnt(4)
	v_mov_b32_e32 v92, v100
	v_mov_b32_e32 v93, v101
	v_mov_b32_e32 v94, v102
	v_mov_b32_e32 v95, v103
	v_mov_b32_e32 v96, v104
	v_mov_b32_e32 v97, v105
	v_mov_b32_e32 v98, v106
	v_mov_b32_e32 v99, v107
	s_add_u32 s48, s48, 0x14000
	s_addc_u32 s49, s49, 0
	ds_read_b128 v[160:163], v10 offset:9216
	ds_read_b128 v[164:167], v10 offset:9280
	ds_read_b128 v[168:171], v10 offset:11520
	ds_read_b128 v[172:175], v10 offset:11584
	ds_read_b128 v[176:179], v10 offset:13824
	ds_read_b128 v[180:183], v10 offset:13888
	ds_read_b128 v[184:187], v10 offset:16128
	ds_read_b128 v[188:191], v10 offset:16192
	ds_read_b128 v[192:195], v10 offset:18432
	ds_read_b128 v[196:199], v10 offset:18496
	s_waitcnt vmcnt(4)
	global_load_dwordx4 v[100:103], v8, s[48:49]
	global_load_dwordx4 v[104:107], v8, s[48:49] offset:64
	v_lshlrev_b32_e32 v234, 16, v92
	v_and_b32_e32 v235, 0xffff0000, v92
	v_pk_mul_f32 v[232:233], v[234:235], v[234:235]
	v_lshlrev_b32_e32 v234, 16, v93
	v_and_b32_e32 v235, 0xffff0000, v93
	v_pk_fma_f32 v[232:233], v[234:235], v[234:235], v[232:233]
	v_lshlrev_b32_e32 v234, 16, v94
	v_and_b32_e32 v235, 0xffff0000, v94
	v_pk_fma_f32 v[232:233], v[234:235], v[234:235], v[232:233]
	v_lshlrev_b32_e32 v234, 16, v95
	v_and_b32_e32 v235, 0xffff0000, v95
	v_pk_fma_f32 v[232:233], v[234:235], v[234:235], v[232:233]
	v_lshlrev_b32_e32 v234, 16, v96
	v_and_b32_e32 v235, 0xffff0000, v96
	v_pk_fma_f32 v[232:233], v[234:235], v[234:235], v[232:233]
	v_lshlrev_b32_e32 v234, 16, v97
	v_and_b32_e32 v235, 0xffff0000, v97
	v_pk_fma_f32 v[232:233], v[234:235], v[234:235], v[232:233]
	v_lshlrev_b32_e32 v234, 16, v98
	v_and_b32_e32 v235, 0xffff0000, v98
	v_pk_fma_f32 v[232:233], v[234:235], v[234:235], v[232:233]
	v_lshlrev_b32_e32 v234, 16, v99
	v_and_b32_e32 v235, 0xffff0000, v99
	v_pk_fma_f32 v[232:233], v[234:235], v[234:235], v[232:233]
	ds_read_b128 v[200:203], v10 offset:20736
	ds_read_b128 v[204:207], v10 offset:20800
	ds_read_b128 v[208:211], v10 offset:23040
	ds_read_b128 v[212:215], v10 offset:23104
	ds_read_b128 v[216:219], v10 offset:25344
	ds_read_b128 v[220:223], v10 offset:25408
	ds_read_b128 v[224:227], v10 offset:27648
	ds_read_b128 v[228:231], v10 offset:27712
	v_add_f32_e32 v232, v232, v233
	s_nop 0
	ds_bpermute_b32 v233, v15, v232
	s_waitcnt lgkmcnt(9)
	v_mfma_f32_16x16x32_bf16 v[108:111], v[160:163], v[92:95], 0
	v_mfma_f32_16x16x32_bf16 v[112:115], v[168:171], v[92:95], 0
	v_mfma_f32_16x16x32_bf16 v[116:119], v[176:179], v[92:95], 0
	v_mfma_f32_16x16x32_bf16 v[120:123], v[184:187], v[92:95], 0
	v_mfma_f32_16x16x32_bf16 v[124:127], v[192:195], v[92:95], 0
	v_mfma_f32_16x16x32_bf16 v[108:111], v[164:167], v[96:99], v[108:111]
	v_mfma_f32_16x16x32_bf16 v[112:115], v[172:175], v[96:99], v[112:115]
	v_mfma_f32_16x16x32_bf16 v[116:119], v[180:183], v[96:99], v[116:119]
	v_mfma_f32_16x16x32_bf16 v[120:123], v[188:191], v[96:99], v[120:123]
	v_mfma_f32_16x16x32_bf16 v[124:127], v[196:199], v[96:99], v[124:127]
	s_waitcnt lgkmcnt(0)
	v_add_f32_e32 v232, v232, v233
	v_mfma_f32_16x16x32_bf16 v[128:131], v[200:203], v[92:95], 0
	v_mfma_f32_16x16x32_bf16 v[132:135], v[208:211], v[92:95], 0
	v_mfma_f32_16x16x32_bf16 v[136:139], v[216:219], v[92:95], 0
	v_mfma_f32_16x16x32_bf16 v[140:143], v[224:227], v[92:95], 0
	ds_bpermute_b32 v233, v16, v232
	v_mfma_f32_16x16x32_bf16 v[128:131], v[204:207], v[96:99], v[128:131]
	v_mfma_f32_16x16x32_bf16 v[132:135], v[212:215], v[96:99], v[132:135]
	v_mfma_f32_16x16x32_bf16 v[136:139], v[220:223], v[96:99], v[136:139]
	v_mfma_f32_16x16x32_bf16 v[140:143], v[228:231], v[96:99], v[140:143]
	ds_read2_b64 v[160:163], v11 offset0:16 offset1:20
	ds_read2_b64 v[164:167], v12 offset0:16 offset1:20
	ds_read2_b64 v[168:171], v13 offset0:16 offset1:20
	ds_read2_b64 v[172:175], v14 offset0:16 offset1:20
	ds_read2_b64 v[176:179], v11 offset0:24 offset1:28
	ds_read2_b64 v[180:183], v12 offset0:24 offset1:28
	ds_read2_b64 v[184:187], v13 offset0:24 offset1:28
	ds_read2_b64 v[188:191], v14 offset0:24 offset1:28
	ds_read2_b64 v[192:195], v11 offset0:32 offset1:36
	ds_read2_b64 v[196:199], v12 offset0:32 offset1:36
	ds_read2_b64 v[200:203], v13 offset0:32 offset1:36
	ds_read2_b64 v[204:207], v14 offset0:32 offset1:36
	s_waitcnt lgkmcnt(12)
	v_add_f32_e32 v232, v232, v233
	v_mul_f32_e32 v232, 0x3c800000, v232
	v_add_f32_e32 v232, 0x358637bd, v232
	v_rsq_f32_e32 v236, v232
	s_nop 0
	v_mov_b32_e32 v237, v236
	s_nop 1
	v_pk_fma_f32 v[108:109], v[108:109], v[236:237], v[52:53]
	v_pk_fma_f32 v[110:111], v[110:111], v[236:237], v[54:55]
	v_pk_fma_f32 v[112:113], v[112:113], v[236:237], v[56:57]
	v_pk_fma_f32 v[114:115], v[114:115], v[236:237], v[58:59]
	v_pk_fma_f32 v[116:117], v[116:117], v[236:237], v[60:61]
	v_pk_fma_f32 v[118:119], v[118:119], v[236:237], v[62:63]
	v_pk_fma_f32 v[120:121], v[120:121], v[236:237], v[64:65]
	v_pk_fma_f32 v[122:123], v[122:123], v[236:237], v[66:67]
	v_pk_fma_f32 v[124:125], v[124:125], v[236:237], v[68:69]
	v_pk_fma_f32 v[126:127], v[126:127], v[236:237], v[70:71]
	v_pk_fma_f32 v[128:129], v[128:129], v[236:237], v[72:73]
	v_pk_fma_f32 v[130:131], v[130:131], v[236:237], v[74:75]
	v_pk_fma_f32 v[132:133], v[132:133], v[236:237], v[76:77]
	v_pk_fma_f32 v[134:135], v[134:135], v[236:237], v[78:79]
	v_pk_fma_f32 v[136:137], v[136:137], v[236:237], v[80:81]
	v_pk_fma_f32 v[138:139], v[138:139], v[236:237], v[82:83]
	v_pk_fma_f32 v[140:141], v[140:141], v[236:237], v[84:85]
	v_pk_fma_f32 v[142:143], v[142:143], v[236:237], v[86:87]
	v_exp_f32_e32 v108, v108
	v_exp_f32_e32 v109, v109
	v_exp_f32_e32 v110, v110
	v_exp_f32_e32 v111, v111
	v_exp_f32_e32 v112, v112
	v_exp_f32_e32 v113, v113
	v_exp_f32_e32 v114, v114
	v_exp_f32_e32 v115, v115
	v_exp_f32_e32 v116, v116
	v_exp_f32_e32 v117, v117
	v_exp_f32_e32 v118, v118
	v_exp_f32_e32 v119, v119
	v_exp_f32_e32 v120, v120
	v_exp_f32_e32 v121, v121
	v_exp_f32_e32 v122, v122
	v_exp_f32_e32 v123, v123
	v_exp_f32_e32 v124, v124
	v_exp_f32_e32 v125, v125
	v_exp_f32_e32 v126, v126
	v_exp_f32_e32 v127, v127
	v_exp_f32_e32 v128, v128
	v_exp_f32_e32 v129, v129
	v_exp_f32_e32 v130, v130
	v_exp_f32_e32 v131, v131
	v_exp_f32_e32 v132, v132
	v_exp_f32_e32 v133, v133
	v_exp_f32_e32 v134, v134
	v_exp_f32_e32 v135, v135
	v_exp_f32_e32 v136, v136
	v_exp_f32_e32 v137, v137
	v_exp_f32_e32 v138, v138
	v_exp_f32_e32 v139, v139
	v_exp_f32_e32 v140, v140
	v_exp_f32_e32 v141, v141
	v_exp_f32_e32 v142, v142
	v_exp_f32_e32 v143, v143
	s_cmp_lg_u32 s36, 0
	s_cbranch_scc1 .Lat_m4
	v_mov_b32_e32 v108, 0
	v_mov_b32_e32 v109, 0
	v_mov_b32_e32 v110, 0
	v_mov_b32_e32 v111, 0
	v_mov_b32_e32 v112, 0
	v_mov_b32_e32 v113, 0
	v_mov_b32_e32 v114, 0
	v_mov_b32_e32 v115, 0
	v_mov_b32_e32 v116, 0
	v_mov_b32_e32 v117, 0
	v_mov_b32_e32 v118, 0
	v_mov_b32_e32 v119, 0
	v_mov_b32_e32 v120, 0
	v_mov_b32_e32 v121, 0
	v_mov_b32_e32 v122, 0
	v_mov_b32_e32 v123, 0
.Lat_m4:
	s_nop 0
	v_pk_add_f32 v[232:233], v[108:109], v[110:111]
	v_pk_add_f32 v[234:235], v[112:113], v[114:115]
	v_pk_add_f32 v[232:233], v[232:233], v[116:117]
	v_pk_add_f32 v[234:235], v[234:235], v[118:119]
	v_pk_add_f32 v[232:233], v[232:233], v[120:121]
	v_pk_add_f32 v[234:235], v[234:235], v[122:123]
	v_pk_add_f32 v[232:233], v[232:233], v[124:125]
	v_pk_add_f32 v[234:235], v[234:235], v[126:127]
	v_pk_add_f32 v[232:233], v[232:233], v[128:129]
	v_pk_add_f32 v[234:235], v[234:235], v[130:131]
	v_pk_add_f32 v[232:233], v[232:233], v[132:133]
	v_pk_add_f32 v[234:235], v[234:235], v[134:135]
	v_pk_add_f32 v[232:233], v[232:233], v[136:137]
	v_pk_add_f32 v[234:235], v[234:235], v[138:139]
	v_pk_add_f32 v[232:233], v[232:233], v[140:141]
	v_pk_add_f32 v[234:235], v[234:235], v[142:143]
	v_pk_add_f32 v[232:233], v[232:233], v[234:235]
	s_nop 0
	v_add_f32_e32 v232, v232, v233
	v_cvt_pk_bf16_f32 v108, v108, v109
	v_cvt_pk_bf16_f32 v109, v110, v111
	v_cvt_pk_bf16_f32 v110, v112, v113
	v_cvt_pk_bf16_f32 v111, v114, v115
	v_cvt_pk_bf16_f32 v116, v116, v117
	v_cvt_pk_bf16_f32 v117, v118, v119
	v_cvt_pk_bf16_f32 v118, v120, v121
	v_cvt_pk_bf16_f32 v119, v122, v123
	v_cvt_pk_bf16_f32 v124, v124, v125
	v_cvt_pk_bf16_f32 v125, v126, v127
	v_cvt_pk_bf16_f32 v126, v128, v129
	v_cvt_pk_bf16_f32 v127, v130, v131
	v_cvt_pk_bf16_f32 v132, v132, v133
	v_cvt_pk_bf16_f32 v133, v134, v135
	v_cvt_pk_bf16_f32 v134, v136, v137
	v_cvt_pk_bf16_f32 v135, v138, v139
	v_cvt_pk_bf16_f32 v140, v140, v141
	v_cvt_pk_bf16_f32 v141, v142, v143
	v_mov_b32_e32 v142, 0
	v_mov_b32_e32 v143, 0
	ds_bpermute_b32 v233, v15, v232
	s_waitcnt lgkmcnt(1)
	v_mfma_f32_16x16x32_bf16 v[144:147], v[160:163], v[108:111], 0
	v_mfma_f32_16x16x32_bf16 v[148:151], v[164:167], v[108:111], 0
	v_mfma_f32_16x16x32_bf16 v[152:155], v[168:171], v[108:111], 0
	v_mfma_f32_16x16x32_bf16 v[156:159], v[172:175], v[108:111], 0
	v_mfma_f32_16x16x32_bf16 v[144:147], v[176:179], v[116:119], v[144:147]
	v_mfma_f32_16x16x32_bf16 v[148:151], v[180:183], v[116:119], v[148:151]
	v_mfma_f32_16x16x32_bf16 v[152:155], v[184:187], v[116:119], v[152:155]
	v_mfma_f32_16x16x32_bf16 v[156:159], v[188:191], v[116:119], v[156:159]
	v_mfma_f32_16x16x32_bf16 v[144:147], v[192:195], v[124:127], v[144:147]
	v_mfma_f32_16x16x32_bf16 v[148:151], v[196:199], v[124:127], v[148:151]
	v_mfma_f32_16x16x32_bf16 v[152:155], v[200:203], v[124:127], v[152:155]
	v_mfma_f32_16x16x32_bf16 v[156:159], v[204:207], v[124:127], v[156:159]
	ds_read2_b64 v[160:163], v11 offset0:40 offset1:44
	ds_read2_b64 v[164:167], v12 offset0:40 offset1:44
	ds_read2_b64 v[168:171], v13 offset0:40 offset1:44
	ds_read2_b64 v[172:175], v14 offset0:40 offset1:44
	ds_read2_b64 v[176:179], v11 offset0:48 offset1:48
	ds_read2_b64 v[180:183], v12 offset0:48 offset1:48
	ds_read2_b64 v[184:187], v13 offset0:48 offset1:48
	ds_read2_b64 v[188:191], v14 offset0:48 offset1:48
	s_waitcnt lgkmcnt(8)
	v_add_f32_e32 v232, v232, v233
	s_nop 0
	ds_bpermute_b32 v233, v16, v232
	s_waitcnt lgkmcnt(1)
	v_mfma_f32_16x16x32_bf16 v[144:147], v[160:163], v[132:135], v[144:147]
	v_mfma_f32_16x16x32_bf16 v[148:151], v[164:167], v[132:135], v[148:151]
	v_mfma_f32_16x16x32_bf16 v[152:155], v[168:171], v[132:135], v[152:155]
	v_mfma_f32_16x16x32_bf16 v[156:159], v[172:175], v[132:135], v[156:159]
	v_mfma_f32_16x16x32_bf16 v[144:147], v[176:179], v[140:143], v[144:147]
	v_mfma_f32_16x16x32_bf16 v[148:151], v[180:183], v[140:143], v[148:151]
	v_mfma_f32_16x16x32_bf16 v[152:155], v[184:187], v[140:143], v[152:155]
	v_mfma_f32_16x16x32_bf16 v[156:159], v[188:191], v[140:143], v[156:159]
	s_waitcnt lgkmcnt(0)
	v_add_f32_e32 v232, v232, v233
	v_add_f32_e32 v232, v232, v88
	v_rcp_f32_e32 v236, v232
	s_nop 0
	v_mov_b32_e32 v237, v236
	s_nop 4
	v_pk_mul_f32 v[144:145], v[144:145], v[236:237]
	v_pk_mul_f32 v[146:147], v[146:147], v[236:237]
	v_pk_mul_f32 v[148:149], v[148:149], v[236:237]
	v_pk_mul_f32 v[150:151], v[150:151], v[236:237]
	v_pk_mul_f32 v[152:153], v[152:153], v[236:237]
	v_pk_mul_f32 v[154:155], v[154:155], v[236:237]
	v_pk_mul_f32 v[156:157], v[156:157], v[236:237]
	v_pk_mul_f32 v[158:159], v[158:159], v[236:237]
	v_cvt_pk_bf16_f32 v144, v144, v145
	v_cvt_pk_bf16_f32 v145, v146, v147
	v_cvt_pk_bf16_f32 v148, v148, v149
	v_cvt_pk_bf16_f32 v149, v150, v151
	v_cvt_pk_bf16_f32 v152, v152, v153
	v_cvt_pk_bf16_f32 v153, v154, v155
	v_cvt_pk_bf16_f32 v156, v156, v157
	v_cvt_pk_bf16_f32 v157, v158, v159
	global_store_dwordx2 v9, v[144:145], s[50:51] offset:0
	global_store_dwordx2 v9, v[148:149], s[50:51] offset:32
	global_store_dwordx2 v9, v[152:153], s[50:51] offset:64
	global_store_dwordx2 v9, v[156:157], s[50:51] offset:96
	s_add_u32 s50, s50, 0x10000
	s_addc_u32 s51, s51, 0
	s_waitcnt vmcnt(4)
	v_mov_b32_e32 v92, v100
	v_mov_b32_e32 v93, v101
	v_mov_b32_e32 v94, v102
	v_mov_b32_e32 v95, v103
	v_mov_b32_e32 v96, v104
	v_mov_b32_e32 v97, v105
	v_mov_b32_e32 v98, v106
	v_mov_b32_e32 v99, v107
	s_add_u32 s48, s48, 0x14000
	s_addc_u32 s49, s49, 0
	ds_read_b128 v[160:163], v10 offset:11520
	ds_read_b128 v[164:167], v10 offset:11584
	ds_read_b128 v[168:171], v10 offset:13824
	ds_read_b128 v[172:175], v10 offset:13888
	ds_read_b128 v[176:179], v10 offset:16128
	ds_read_b128 v[180:183], v10 offset:16192
	ds_read_b128 v[184:187], v10 offset:18432
	ds_read_b128 v[188:191], v10 offset:18496
	ds_read_b128 v[192:195], v10 offset:20736
	ds_read_b128 v[196:199], v10 offset:20800
	s_waitcnt vmcnt(4)
	global_load_dwordx4 v[100:103], v8, s[48:49]
	global_load_dwordx4 v[104:107], v8, s[48:49] offset:64
	v_lshlrev_b32_e32 v234, 16, v92
	v_and_b32_e32 v235, 0xffff0000, v92
	v_pk_mul_f32 v[232:233], v[234:235], v[234:235]
	v_lshlrev_b32_e32 v234, 16, v93
	v_and_b32_e32 v235, 0xffff0000, v93
	v_pk_fma_f32 v[232:233], v[234:235], v[234:235], v[232:233]
	v_lshlrev_b32_e32 v234, 16, v94
	v_and_b32_e32 v235, 0xffff0000, v94
	v_pk_fma_f32 v[232:233], v[234:235], v[234:235], v[232:233]
	v_lshlrev_b32_e32 v234, 16, v95
	v_and_b32_e32 v235, 0xffff0000, v95
	v_pk_fma_f32 v[232:233], v[234:235], v[234:235], v[232:233]
	v_lshlrev_b32_e32 v234, 16, v96
	v_and_b32_e32 v235, 0xffff0000, v96
	v_pk_fma_f32 v[232:233], v[234:235], v[234:235], v[232:233]
	v_lshlrev_b32_e32 v234, 16, v97
	v_and_b32_e32 v235, 0xffff0000, v97
	v_pk_fma_f32 v[232:233], v[234:235], v[234:235], v[232:233]
	v_lshlrev_b32_e32 v234, 16, v98
	v_and_b32_e32 v235, 0xffff0000, v98
	v_pk_fma_f32 v[232:233], v[234:235], v[234:235], v[232:233]
	v_lshlrev_b32_e32 v234, 16, v99
	v_and_b32_e32 v235, 0xffff0000, v99
	v_pk_fma_f32 v[232:233], v[234:235], v[234:235], v[232:233]
	ds_read_b128 v[200:203], v10 offset:23040
	ds_read_b128 v[204:207], v10 offset:23104
	ds_read_b128 v[208:211], v10 offset:25344
	ds_read_b128 v[212:215], v10 offset:25408
	ds_read_b128 v[216:219], v10 offset:27648
	ds_read_b128 v[220:223], v10 offset:27712
	ds_read_b128 v[224:227], v10 offset:29952
	ds_read_b128 v[228:231], v10 offset:30016
	v_add_f32_e32 v232, v232, v233
	s_nop 0
	ds_bpermute_b32 v233, v15, v232
	s_waitcnt lgkmcnt(9)
	v_mfma_f32_16x16x32_bf16 v[108:111], v[160:163], v[92:95], 0
	v_mfma_f32_16x16x32_bf16 v[112:115], v[168:171], v[92:95], 0
	v_mfma_f32_16x16x32_bf16 v[116:119], v[176:179], v[92:95], 0
	v_mfma_f32_16x16x32_bf16 v[120:123], v[184:187], v[92:95], 0
	v_mfma_f32_16x16x32_bf16 v[124:127], v[192:195], v[92:95], 0
	v_mfma_f32_16x16x32_bf16 v[108:111], v[164:167], v[96:99], v[108:111]
	v_mfma_f32_16x16x32_bf16 v[112:115], v[172:175], v[96:99], v[112:115]
	v_mfma_f32_16x16x32_bf16 v[116:119], v[180:183], v[96:99], v[116:119]
	v_mfma_f32_16x16x32_bf16 v[120:123], v[188:191], v[96:99], v[120:123]
	v_mfma_f32_16x16x32_bf16 v[124:127], v[196:199], v[96:99], v[124:127]
	s_waitcnt lgkmcnt(0)
	v_add_f32_e32 v232, v232, v233
	v_mfma_f32_16x16x32_bf16 v[128:131], v[200:203], v[92:95], 0
	v_mfma_f32_16x16x32_bf16 v[132:135], v[208:211], v[92:95], 0
	v_mfma_f32_16x16x32_bf16 v[136:139], v[216:219], v[92:95], 0
	v_mfma_f32_16x16x32_bf16 v[140:143], v[224:227], v[92:95], 0
	ds_bpermute_b32 v233, v16, v232
	v_mfma_f32_16x16x32_bf16 v[128:131], v[204:207], v[96:99], v[128:131]
	v_mfma_f32_16x16x32_bf16 v[132:135], v[212:215], v[96:99], v[132:135]
	v_mfma_f32_16x16x32_bf16 v[136:139], v[220:223], v[96:99], v[136:139]
	v_mfma_f32_16x16x32_bf16 v[140:143], v[228:231], v[96:99], v[140:143]
	ds_read2_b64 v[160:163], v11 offset0:20 offset1:24
	ds_read2_b64 v[164:167], v12 offset0:20 offset1:24
	ds_read2_b64 v[168:171], v13 offset0:20 offset1:24
	ds_read2_b64 v[172:175], v14 offset0:20 offset1:24
	ds_read2_b64 v[176:179], v11 offset0:28 offset1:32
	ds_read2_b64 v[180:183], v12 offset0:28 offset1:32
	ds_read2_b64 v[184:187], v13 offset0:28 offset1:32
	ds_read2_b64 v[188:191], v14 offset0:28 offset1:32
	ds_read2_b64 v[192:195], v11 offset0:36 offset1:40
	ds_read2_b64 v[196:199], v12 offset0:36 offset1:40
	ds_read2_b64 v[200:203], v13 offset0:36 offset1:40
	ds_read2_b64 v[204:207], v14 offset0:36 offset1:40
	s_waitcnt lgkmcnt(12)
	v_add_f32_e32 v232, v232, v233
	v_mul_f32_e32 v232, 0x3c800000, v232
	v_add_f32_e32 v232, 0x358637bd, v232
	v_rsq_f32_e32 v236, v232
	s_nop 0
	v_mov_b32_e32 v237, v236
	s_nop 1
	v_pk_fma_f32 v[108:109], v[108:109], v[236:237], v[52:53]
	v_pk_fma_f32 v[110:111], v[110:111], v[236:237], v[54:55]
	v_pk_fma_f32 v[112:113], v[112:113], v[236:237], v[56:57]
	v_pk_fma_f32 v[114:115], v[114:115], v[236:237], v[58:59]
	v_pk_fma_f32 v[116:117], v[116:117], v[236:237], v[60:61]
	v_pk_fma_f32 v[118:119], v[118:119], v[236:237], v[62:63]
	v_pk_fma_f32 v[120:121], v[120:121], v[236:237], v[64:65]
	v_pk_fma_f32 v[122:123], v[122:123], v[236:237], v[66:67]
	v_pk_fma_f32 v[124:125], v[124:125], v[236:237], v[68:69]
	v_pk_fma_f32 v[126:127], v[126:127], v[236:237], v[70:71]
	v_pk_fma_f32 v[128:129], v[128:129], v[236:237], v[72:73]
	v_pk_fma_f32 v[130:131], v[130:131], v[236:237], v[74:75]
	v_pk_fma_f32 v[132:133], v[132:133], v[236:237], v[76:77]
	v_pk_fma_f32 v[134:135], v[134:135], v[236:237], v[78:79]
	v_pk_fma_f32 v[136:137], v[136:137], v[236:237], v[80:81]
	v_pk_fma_f32 v[138:139], v[138:139], v[236:237], v[82:83]
	v_pk_fma_f32 v[140:141], v[140:141], v[236:237], v[84:85]
	v_pk_fma_f32 v[142:143], v[142:143], v[236:237], v[86:87]
	v_exp_f32_e32 v108, v108
	v_exp_f32_e32 v109, v109
	v_exp_f32_e32 v110, v110
	v_exp_f32_e32 v111, v111
	v_exp_f32_e32 v112, v112
	v_exp_f32_e32 v113, v113
	v_exp_f32_e32 v114, v114
	v_exp_f32_e32 v115, v115
	v_exp_f32_e32 v116, v116
	v_exp_f32_e32 v117, v117
	v_exp_f32_e32 v118, v118
	v_exp_f32_e32 v119, v119
	v_exp_f32_e32 v120, v120
	v_exp_f32_e32 v121, v121
	v_exp_f32_e32 v122, v122
	v_exp_f32_e32 v123, v123
	v_exp_f32_e32 v124, v124
	v_exp_f32_e32 v125, v125
	v_exp_f32_e32 v126, v126
	v_exp_f32_e32 v127, v127
	v_exp_f32_e32 v128, v128
	v_exp_f32_e32 v129, v129
	v_exp_f32_e32 v130, v130
	v_exp_f32_e32 v131, v131
	v_exp_f32_e32 v132, v132
	v_exp_f32_e32 v133, v133
	v_exp_f32_e32 v134, v134
	v_exp_f32_e32 v135, v135
	v_exp_f32_e32 v136, v136
	v_exp_f32_e32 v137, v137
	v_exp_f32_e32 v138, v138
	v_exp_f32_e32 v139, v139
	v_exp_f32_e32 v140, v140
	v_exp_f32_e32 v141, v141
	v_exp_f32_e32 v142, v142
	v_exp_f32_e32 v143, v143
	s_cmp_lg_u32 s36, 0
	s_cbranch_scc1 .Lat_m5
	v_mov_b32_e32 v108, 0
	v_mov_b32_e32 v109, 0
	v_mov_b32_e32 v110, 0
	v_mov_b32_e32 v111, 0
	v_mov_b32_e32 v112, 0
	v_mov_b32_e32 v113, 0
	v_mov_b32_e32 v114, 0
	v_mov_b32_e32 v115, 0
	v_mov_b32_e32 v116, 0
	v_mov_b32_e32 v117, 0
	v_mov_b32_e32 v118, 0
	v_mov_b32_e32 v119, 0
.Lat_m5:
	s_nop 0
	v_pk_add_f32 v[232:233], v[108:109], v[110:111]
	v_pk_add_f32 v[234:235], v[112:113], v[114:115]
	v_pk_add_f32 v[232:233], v[232:233], v[116:117]
	v_pk_add_f32 v[234:235], v[234:235], v[118:119]
	v_pk_add_f32 v[232:233], v[232:233], v[120:121]
	v_pk_add_f32 v[234:235], v[234:235], v[122:123]
	v_pk_add_f32 v[232:233], v[232:233], v[124:125]
	v_pk_add_f32 v[234:235], v[234:235], v[126:127]
	v_pk_add_f32 v[232:233], v[232:233], v[128:129]
	v_pk_add_f32 v[234:235], v[234:235], v[130:131]
	v_pk_add_f32 v[232:233], v[232:233], v[132:133]
	v_pk_add_f32 v[234:235], v[234:235], v[134:135]
	v_pk_add_f32 v[232:233], v[232:233], v[136:137]
	v_pk_add_f32 v[234:235], v[234:235], v[138:139]
	v_pk_add_f32 v[232:233], v[232:233], v[140:141]
	v_pk_add_f32 v[234:235], v[234:235], v[142:143]
	v_pk_add_f32 v[232:233], v[232:233], v[234:235]
	s_nop 0
	v_add_f32_e32 v232, v232, v233
	v_cvt_pk_bf16_f32 v108, v108, v109
	v_cvt_pk_bf16_f32 v109, v110, v111
	v_cvt_pk_bf16_f32 v110, v112, v113
	v_cvt_pk_bf16_f32 v111, v114, v115
	v_cvt_pk_bf16_f32 v116, v116, v117
	v_cvt_pk_bf16_f32 v117, v118, v119
	v_cvt_pk_bf16_f32 v118, v120, v121
	v_cvt_pk_bf16_f32 v119, v122, v123
	v_cvt_pk_bf16_f32 v124, v124, v125
	v_cvt_pk_bf16_f32 v125, v126, v127
	v_cvt_pk_bf16_f32 v126, v128, v129
	v_cvt_pk_bf16_f32 v127, v130, v131
	v_cvt_pk_bf16_f32 v132, v132, v133
	v_cvt_pk_bf16_f32 v133, v134, v135
	v_cvt_pk_bf16_f32 v134, v136, v137
	v_cvt_pk_bf16_f32 v135, v138, v139
	v_cvt_pk_bf16_f32 v140, v140, v141
	v_cvt_pk_bf16_f32 v141, v142, v143
	v_mov_b32_e32 v142, 0
	v_mov_b32_e32 v143, 0
	ds_bpermute_b32 v233, v15, v232
	s_waitcnt lgkmcnt(1)
	v_mfma_f32_16x16x32_bf16 v[144:147], v[160:163], v[108:111], 0
	v_mfma_f32_16x16x32_bf16 v[148:151], v[164:167], v[108:111], 0
	v_mfma_f32_16x16x32_bf16 v[152:155], v[168:171], v[108:111], 0
	v_mfma_f32_16x16x32_bf16 v[156:159], v[172:175], v[108:111], 0
	v_mfma_f32_16x16x32_bf16 v[144:147], v[176:179], v[116:119], v[144:147]
	v_mfma_f32_16x16x32_bf16 v[148:151], v[180:183], v[116:119], v[148:151]
	v_mfma_f32_16x16x32_bf16 v[152:155], v[184:187], v[116:119], v[152:155]
	v_mfma_f32_16x16x32_bf16 v[156:159], v[188:191], v[116:119], v[156:159]
	v_mfma_f32_16x16x32_bf16 v[144:147], v[192:195], v[124:127], v[144:147]
	v_mfma_f32_16x16x32_bf16 v[148:151], v[196:199], v[124:127], v[148:151]
	v_mfma_f32_16x16x32_bf16 v[152:155], v[200:203], v[124:127], v[152:155]
	v_mfma_f32_16x16x32_bf16 v[156:159], v[204:207], v[124:127], v[156:159]
	ds_read2_b64 v[160:163], v11 offset0:44 offset1:48
	ds_read2_b64 v[164:167], v12 offset0:44 offset1:48
	ds_read2_b64 v[168:171], v13 offset0:44 offset1:48
	ds_read2_b64 v[172:175], v14 offset0:44 offset1:48
	ds_read2_b64 v[176:179], v11 offset0:52 offset1:52
	ds_read2_b64 v[180:183], v12 offset0:52 offset1:52
	ds_read2_b64 v[184:187], v13 offset0:52 offset1:52
	ds_read2_b64 v[188:191], v14 offset0:52 offset1:52
	s_waitcnt lgkmcnt(8)
	v_add_f32_e32 v232, v232, v233
	s_nop 0
	ds_bpermute_b32 v233, v16, v232
	s_waitcnt lgkmcnt(1)
	v_mfma_f32_16x16x32_bf16 v[144:147], v[160:163], v[132:135], v[144:147]
	v_mfma_f32_16x16x32_bf16 v[148:151], v[164:167], v[132:135], v[148:151]
	v_mfma_f32_16x16x32_bf16 v[152:155], v[168:171], v[132:135], v[152:155]
	v_mfma_f32_16x16x32_bf16 v[156:159], v[172:175], v[132:135], v[156:159]
	v_mfma_f32_16x16x32_bf16 v[144:147], v[176:179], v[140:143], v[144:147]
	v_mfma_f32_16x16x32_bf16 v[148:151], v[180:183], v[140:143], v[148:151]
	v_mfma_f32_16x16x32_bf16 v[152:155], v[184:187], v[140:143], v[152:155]
	v_mfma_f32_16x16x32_bf16 v[156:159], v[188:191], v[140:143], v[156:159]
	s_waitcnt lgkmcnt(0)
	v_add_f32_e32 v232, v232, v233
	v_add_f32_e32 v232, v232, v88
	v_rcp_f32_e32 v236, v232
	s_nop 0
	v_mov_b32_e32 v237, v236
	s_nop 4
	v_pk_mul_f32 v[144:145], v[144:145], v[236:237]
	v_pk_mul_f32 v[146:147], v[146:147], v[236:237]
	v_pk_mul_f32 v[148:149], v[148:149], v[236:237]
	v_pk_mul_f32 v[150:151], v[150:151], v[236:237]
	v_pk_mul_f32 v[152:153], v[152:153], v[236:237]
	v_pk_mul_f32 v[154:155], v[154:155], v[236:237]
	v_pk_mul_f32 v[156:157], v[156:157], v[236:237]
	v_pk_mul_f32 v[158:159], v[158:159], v[236:237]
	v_cvt_pk_bf16_f32 v144, v144, v145
	v_cvt_pk_bf16_f32 v145, v146, v147
	v_cvt_pk_bf16_f32 v148, v148, v149
	v_cvt_pk_bf16_f32 v149, v150, v151
	v_cvt_pk_bf16_f32 v152, v152, v153
	v_cvt_pk_bf16_f32 v153, v154, v155
	v_cvt_pk_bf16_f32 v156, v156, v157
	v_cvt_pk_bf16_f32 v157, v158, v159
	global_store_dwordx2 v9, v[144:145], s[50:51] offset:0
	global_store_dwordx2 v9, v[148:149], s[50:51] offset:32
	global_store_dwordx2 v9, v[152:153], s[50:51] offset:64
	global_store_dwordx2 v9, v[156:157], s[50:51] offset:96
	s_add_u32 s50, s50, 0x10000
	s_addc_u32 s51, s51, 0
	s_waitcnt vmcnt(4)
	v_mov_b32_e32 v92, v100
	v_mov_b32_e32 v93, v101
	v_mov_b32_e32 v94, v102
	v_mov_b32_e32 v95, v103
	v_mov_b32_e32 v96, v104
	v_mov_b32_e32 v97, v105
	v_mov_b32_e32 v98, v106
	v_mov_b32_e32 v99, v107
	s_add_u32 s48, s48, 0x14000
	s_addc_u32 s49, s49, 0
	ds_read_b128 v[160:163], v10 offset:13824
	ds_read_b128 v[164:167], v10 offset:13888
	ds_read_b128 v[168:171], v10 offset:16128
	ds_read_b128 v[172:175], v10 offset:16192
	ds_read_b128 v[176:179], v10 offset:18432
	ds_read_b128 v[180:183], v10 offset:18496
	ds_read_b128 v[184:187], v10 offset:20736
	ds_read_b128 v[188:191], v10 offset:20800
	ds_read_b128 v[192:195], v10 offset:23040
	ds_read_b128 v[196:199], v10 offset:23104
	s_waitcnt vmcnt(4)
	global_load_dwordx4 v[100:103], v8, s[48:49]
	global_load_dwordx4 v[104:107], v8, s[48:49] offset:64
	v_lshlrev_b32_e32 v234, 16, v92
	v_and_b32_e32 v235, 0xffff0000, v92
	v_pk_mul_f32 v[232:233], v[234:235], v[234:235]
	v_lshlrev_b32_e32 v234, 16, v93
	v_and_b32_e32 v235, 0xffff0000, v93
	v_pk_fma_f32 v[232:233], v[234:235], v[234:235], v[232:233]
	v_lshlrev_b32_e32 v234, 16, v94
	v_and_b32_e32 v235, 0xffff0000, v94
	v_pk_fma_f32 v[232:233], v[234:235], v[234:235], v[232:233]
	v_lshlrev_b32_e32 v234, 16, v95
	v_and_b32_e32 v235, 0xffff0000, v95
	v_pk_fma_f32 v[232:233], v[234:235], v[234:235], v[232:233]
	v_lshlrev_b32_e32 v234, 16, v96
	v_and_b32_e32 v235, 0xffff0000, v96
	v_pk_fma_f32 v[232:233], v[234:235], v[234:235], v[232:233]
	v_lshlrev_b32_e32 v234, 16, v97
	v_and_b32_e32 v235, 0xffff0000, v97
	v_pk_fma_f32 v[232:233], v[234:235], v[234:235], v[232:233]
	v_lshlrev_b32_e32 v234, 16, v98
	v_and_b32_e32 v235, 0xffff0000, v98
	v_pk_fma_f32 v[232:233], v[234:235], v[234:235], v[232:233]
	v_lshlrev_b32_e32 v234, 16, v99
	v_and_b32_e32 v235, 0xffff0000, v99
	v_pk_fma_f32 v[232:233], v[234:235], v[234:235], v[232:233]
	ds_read_b128 v[200:203], v10 offset:25344
	ds_read_b128 v[204:207], v10 offset:25408
	ds_read_b128 v[208:211], v10 offset:27648
	ds_read_b128 v[212:215], v10 offset:27712
	ds_read_b128 v[216:219], v10 offset:29952
	ds_read_b128 v[220:223], v10 offset:30016
	ds_read_b128 v[224:227], v10 offset:32256
	ds_read_b128 v[228:231], v10 offset:32320
	v_add_f32_e32 v232, v232, v233
	s_nop 0
	ds_bpermute_b32 v233, v15, v232
	s_waitcnt lgkmcnt(9)
	v_mfma_f32_16x16x32_bf16 v[108:111], v[160:163], v[92:95], 0
	v_mfma_f32_16x16x32_bf16 v[112:115], v[168:171], v[92:95], 0
	v_mfma_f32_16x16x32_bf16 v[116:119], v[176:179], v[92:95], 0
	v_mfma_f32_16x16x32_bf16 v[120:123], v[184:187], v[92:95], 0
	v_mfma_f32_16x16x32_bf16 v[124:127], v[192:195], v[92:95], 0
	v_mfma_f32_16x16x32_bf16 v[108:111], v[164:167], v[96:99], v[108:111]
	v_mfma_f32_16x16x32_bf16 v[112:115], v[172:175], v[96:99], v[112:115]
	v_mfma_f32_16x16x32_bf16 v[116:119], v[180:183], v[96:99], v[116:119]
	v_mfma_f32_16x16x32_bf16 v[120:123], v[188:191], v[96:99], v[120:123]
	v_mfma_f32_16x16x32_bf16 v[124:127], v[196:199], v[96:99], v[124:127]
	s_waitcnt lgkmcnt(0)
	v_add_f32_e32 v232, v232, v233
	v_mfma_f32_16x16x32_bf16 v[128:131], v[200:203], v[92:95], 0
	v_mfma_f32_16x16x32_bf16 v[132:135], v[208:211], v[92:95], 0
	v_mfma_f32_16x16x32_bf16 v[136:139], v[216:219], v[92:95], 0
	v_mfma_f32_16x16x32_bf16 v[140:143], v[224:227], v[92:95], 0
	ds_bpermute_b32 v233, v16, v232
	v_mfma_f32_16x16x32_bf16 v[128:131], v[204:207], v[96:99], v[128:131]
	v_mfma_f32_16x16x32_bf16 v[132:135], v[212:215], v[96:99], v[132:135]
	v_mfma_f32_16x16x32_bf16 v[136:139], v[220:223], v[96:99], v[136:139]
	v_mfma_f32_16x16x32_bf16 v[140:143], v[228:231], v[96:99], v[140:143]
	ds_read2_b64 v[160:163], v11 offset0:24 offset1:28
	ds_read2_b64 v[164:167], v12 offset0:24 offset1:28
	ds_read2_b64 v[168:171], v13 offset0:24 offset1:28
	ds_read2_b64 v[172:175], v14 offset0:24 offset1:28
	ds_read2_b64 v[176:179], v11 offset0:32 offset1:36
	ds_read2_b64 v[180:183], v12 offset0:32 offset1:36
	ds_read2_b64 v[184:187], v13 offset0:32 offset1:36
	ds_read2_b64 v[188:191], v14 offset0:32 offset1:36
	ds_read2_b64 v[192:195], v11 offset0:40 offset1:44
	ds_read2_b64 v[196:199], v12 offset0:40 offset1:44
	ds_read2_b64 v[200:203], v13 offset0:40 offset1:44
	ds_read2_b64 v[204:207], v14 offset0:40 offset1:44
	s_waitcnt lgkmcnt(12)
	v_add_f32_e32 v232, v232, v233
	v_mul_f32_e32 v232, 0x3c800000, v232
	v_add_f32_e32 v232, 0x358637bd, v232
	v_rsq_f32_e32 v236, v232
	s_nop 0
	v_mov_b32_e32 v237, v236
	s_nop 1
	v_pk_fma_f32 v[108:109], v[108:109], v[236:237], v[52:53]
	v_pk_fma_f32 v[110:111], v[110:111], v[236:237], v[54:55]
	v_pk_fma_f32 v[112:113], v[112:113], v[236:237], v[56:57]
	v_pk_fma_f32 v[114:115], v[114:115], v[236:237], v[58:59]
	v_pk_fma_f32 v[116:117], v[116:117], v[236:237], v[60:61]
	v_pk_fma_f32 v[118:119], v[118:119], v[236:237], v[62:63]
	v_pk_fma_f32 v[120:121], v[120:121], v[236:237], v[64:65]
	v_pk_fma_f32 v[122:123], v[122:123], v[236:237], v[66:67]
	v_pk_fma_f32 v[124:125], v[124:125], v[236:237], v[68:69]
	v_pk_fma_f32 v[126:127], v[126:127], v[236:237], v[70:71]
	v_pk_fma_f32 v[128:129], v[128:129], v[236:237], v[72:73]
	v_pk_fma_f32 v[130:131], v[130:131], v[236:237], v[74:75]
	v_pk_fma_f32 v[132:133], v[132:133], v[236:237], v[76:77]
	v_pk_fma_f32 v[134:135], v[134:135], v[236:237], v[78:79]
	v_pk_fma_f32 v[136:137], v[136:137], v[236:237], v[80:81]
	v_pk_fma_f32 v[138:139], v[138:139], v[236:237], v[82:83]
	v_pk_fma_f32 v[140:141], v[140:141], v[236:237], v[84:85]
	v_pk_fma_f32 v[142:143], v[142:143], v[236:237], v[86:87]
	v_exp_f32_e32 v108, v108
	v_exp_f32_e32 v109, v109
	v_exp_f32_e32 v110, v110
	v_exp_f32_e32 v111, v111
	v_exp_f32_e32 v112, v112
	v_exp_f32_e32 v113, v113
	v_exp_f32_e32 v114, v114
	v_exp_f32_e32 v115, v115
	v_exp_f32_e32 v116, v116
	v_exp_f32_e32 v117, v117
	v_exp_f32_e32 v118, v118
	v_exp_f32_e32 v119, v119
	v_exp_f32_e32 v120, v120
	v_exp_f32_e32 v121, v121
	v_exp_f32_e32 v122, v122
	v_exp_f32_e32 v123, v123
	v_exp_f32_e32 v124, v124
	v_exp_f32_e32 v125, v125
	v_exp_f32_e32 v126, v126
	v_exp_f32_e32 v127, v127
	v_exp_f32_e32 v128, v128
	v_exp_f32_e32 v129, v129
	v_exp_f32_e32 v130, v130
	v_exp_f32_e32 v131, v131
	v_exp_f32_e32 v132, v132
	v_exp_f32_e32 v133, v133
	v_exp_f32_e32 v134, v134
	v_exp_f32_e32 v135, v135
	v_exp_f32_e32 v136, v136
	v_exp_f32_e32 v137, v137
	v_exp_f32_e32 v138, v138
	v_exp_f32_e32 v139, v139
	v_exp_f32_e32 v140, v140
	v_exp_f32_e32 v141, v141
	v_exp_f32_e32 v142, v142
	v_exp_f32_e32 v143, v143
	s_cmp_lg_u32 s36, 0
	s_cbranch_scc1 .Lat_m6
	v_mov_b32_e32 v108, 0
	v_mov_b32_e32 v109, 0
	v_mov_b32_e32 v110, 0
	v_mov_b32_e32 v111, 0
	v_mov_b32_e32 v112, 0
	v_mov_b32_e32 v113, 0
	v_mov_b32_e32 v114, 0
	v_mov_b32_e32 v115, 0
.Lat_m6:
	s_nop 0
	v_pk_add_f32 v[232:233], v[108:109], v[110:111]
	v_pk_add_f32 v[234:235], v[112:113], v[114:115]
	v_pk_add_f32 v[232:233], v[232:233], v[116:117]
	v_pk_add_f32 v[234:235], v[234:235], v[118:119]
	v_pk_add_f32 v[232:233], v[232:233], v[120:121]
	v_pk_add_f32 v[234:235], v[234:235], v[122:123]
	v_pk_add_f32 v[232:233], v[232:233], v[124:125]
	v_pk_add_f32 v[234:235], v[234:235], v[126:127]
	v_pk_add_f32 v[232:233], v[232:233], v[128:129]
	v_pk_add_f32 v[234:235], v[234:235], v[130:131]
	v_pk_add_f32 v[232:233], v[232:233], v[132:133]
	v_pk_add_f32 v[234:235], v[234:235], v[134:135]
	v_pk_add_f32 v[232:233], v[232:233], v[136:137]
	v_pk_add_f32 v[234:235], v[234:235], v[138:139]
	v_pk_add_f32 v[232:233], v[232:233], v[140:141]
	v_pk_add_f32 v[234:235], v[234:235], v[142:143]
	v_pk_add_f32 v[232:233], v[232:233], v[234:235]
	s_nop 0
	v_add_f32_e32 v232, v232, v233
	v_cvt_pk_bf16_f32 v108, v108, v109
	v_cvt_pk_bf16_f32 v109, v110, v111
	v_cvt_pk_bf16_f32 v110, v112, v113
	v_cvt_pk_bf16_f32 v111, v114, v115
	v_cvt_pk_bf16_f32 v116, v116, v117
	v_cvt_pk_bf16_f32 v117, v118, v119
	v_cvt_pk_bf16_f32 v118, v120, v121
	v_cvt_pk_bf16_f32 v119, v122, v123
	v_cvt_pk_bf16_f32 v124, v124, v125
	v_cvt_pk_bf16_f32 v125, v126, v127
	v_cvt_pk_bf16_f32 v126, v128, v129
	v_cvt_pk_bf16_f32 v127, v130, v131
	v_cvt_pk_bf16_f32 v132, v132, v133
	v_cvt_pk_bf16_f32 v133, v134, v135
	v_cvt_pk_bf16_f32 v134, v136, v137
	v_cvt_pk_bf16_f32 v135, v138, v139
	v_cvt_pk_bf16_f32 v140, v140, v141
	v_cvt_pk_bf16_f32 v141, v142, v143
	v_mov_b32_e32 v142, 0
	v_mov_b32_e32 v143, 0
	ds_bpermute_b32 v233, v15, v232
	s_waitcnt lgkmcnt(1)
	v_mfma_f32_16x16x32_bf16 v[144:147], v[160:163], v[108:111], 0
	v_mfma_f32_16x16x32_bf16 v[148:151], v[164:167], v[108:111], 0
	v_mfma_f32_16x16x32_bf16 v[152:155], v[168:171], v[108:111], 0
	v_mfma_f32_16x16x32_bf16 v[156:159], v[172:175], v[108:111], 0
	v_mfma_f32_16x16x32_bf16 v[144:147], v[176:179], v[116:119], v[144:147]
	v_mfma_f32_16x16x32_bf16 v[148:151], v[180:183], v[116:119], v[148:151]
	v_mfma_f32_16x16x32_bf16 v[152:155], v[184:187], v[116:119], v[152:155]
	v_mfma_f32_16x16x32_bf16 v[156:159], v[188:191], v[116:119], v[156:159]
	v_mfma_f32_16x16x32_bf16 v[144:147], v[192:195], v[124:127], v[144:147]
	v_mfma_f32_16x16x32_bf16 v[148:151], v[196:199], v[124:127], v[148:151]
	v_mfma_f32_16x16x32_bf16 v[152:155], v[200:203], v[124:127], v[152:155]
	v_mfma_f32_16x16x32_bf16 v[156:159], v[204:207], v[124:127], v[156:159]
	ds_read2_b64 v[160:163], v11 offset0:48 offset1:52
	ds_read2_b64 v[164:167], v12 offset0:48 offset1:52
	ds_read2_b64 v[168:171], v13 offset0:48 offset1:52
	ds_read2_b64 v[172:175], v14 offset0:48 offset1:52
	ds_read2_b64 v[176:179], v11 offset0:56 offset1:56
	ds_read2_b64 v[180:183], v12 offset0:56 offset1:56
	ds_read2_b64 v[184:187], v13 offset0:56 offset1:56
	ds_read2_b64 v[188:191], v14 offset0:56 offset1:56
	s_waitcnt lgkmcnt(8)
	v_add_f32_e32 v232, v232, v233
	s_nop 0
	ds_bpermute_b32 v233, v16, v232
	s_waitcnt lgkmcnt(1)
	v_mfma_f32_16x16x32_bf16 v[144:147], v[160:163], v[132:135], v[144:147]
	v_mfma_f32_16x16x32_bf16 v[148:151], v[164:167], v[132:135], v[148:151]
	v_mfma_f32_16x16x32_bf16 v[152:155], v[168:171], v[132:135], v[152:155]
	v_mfma_f32_16x16x32_bf16 v[156:159], v[172:175], v[132:135], v[156:159]
	v_mfma_f32_16x16x32_bf16 v[144:147], v[176:179], v[140:143], v[144:147]
	v_mfma_f32_16x16x32_bf16 v[148:151], v[180:183], v[140:143], v[148:151]
	v_mfma_f32_16x16x32_bf16 v[152:155], v[184:187], v[140:143], v[152:155]
	v_mfma_f32_16x16x32_bf16 v[156:159], v[188:191], v[140:143], v[156:159]
	s_waitcnt lgkmcnt(0)
	v_add_f32_e32 v232, v232, v233
	v_add_f32_e32 v232, v232, v88
	v_rcp_f32_e32 v236, v232
	s_nop 0
	v_mov_b32_e32 v237, v236
	s_nop 4
	v_pk_mul_f32 v[144:145], v[144:145], v[236:237]
	v_pk_mul_f32 v[146:147], v[146:147], v[236:237]
	v_pk_mul_f32 v[148:149], v[148:149], v[236:237]
	v_pk_mul_f32 v[150:151], v[150:151], v[236:237]
	v_pk_mul_f32 v[152:153], v[152:153], v[236:237]
	v_pk_mul_f32 v[154:155], v[154:155], v[236:237]
	v_pk_mul_f32 v[156:157], v[156:157], v[236:237]
	v_pk_mul_f32 v[158:159], v[158:159], v[236:237]
	v_cvt_pk_bf16_f32 v144, v144, v145
	v_cvt_pk_bf16_f32 v145, v146, v147
	v_cvt_pk_bf16_f32 v148, v148, v149
	v_cvt_pk_bf16_f32 v149, v150, v151
	v_cvt_pk_bf16_f32 v152, v152, v153
	v_cvt_pk_bf16_f32 v153, v154, v155
	v_cvt_pk_bf16_f32 v156, v156, v157
	v_cvt_pk_bf16_f32 v157, v158, v159
	global_store_dwordx2 v9, v[144:145], s[50:51] offset:0
	global_store_dwordx2 v9, v[148:149], s[50:51] offset:32
	global_store_dwordx2 v9, v[152:153], s[50:51] offset:64
	global_store_dwordx2 v9, v[156:157], s[50:51] offset:96
	s_add_u32 s50, s50, 0x10000
	s_addc_u32 s51, s51, 0
	s_waitcnt vmcnt(4)
	v_mov_b32_e32 v92, v100
	v_mov_b32_e32 v93, v101
	v_mov_b32_e32 v94, v102
	v_mov_b32_e32 v95, v103
	v_mov_b32_e32 v96, v104
	v_mov_b32_e32 v97, v105
	v_mov_b32_e32 v98, v106
	v_mov_b32_e32 v99, v107
	ds_read_b128 v[160:163], v10 offset:16128
	ds_read_b128 v[164:167], v10 offset:16192
	ds_read_b128 v[168:171], v10 offset:18432
	ds_read_b128 v[172:175], v10 offset:18496
	ds_read_b128 v[176:179], v10 offset:20736
	ds_read_b128 v[180:183], v10 offset:20800
	ds_read_b128 v[184:187], v10 offset:23040
	ds_read_b128 v[188:191], v10 offset:23104
	ds_read_b128 v[192:195], v10 offset:25344
	ds_read_b128 v[196:199], v10 offset:25408
	s_waitcnt vmcnt(4)
	v_lshlrev_b32_e32 v234, 16, v92
	v_and_b32_e32 v235, 0xffff0000, v92
	v_pk_mul_f32 v[232:233], v[234:235], v[234:235]
	v_lshlrev_b32_e32 v234, 16, v93
	v_and_b32_e32 v235, 0xffff0000, v93
	v_pk_fma_f32 v[232:233], v[234:235], v[234:235], v[232:233]
	v_lshlrev_b32_e32 v234, 16, v94
	v_and_b32_e32 v235, 0xffff0000, v94
	v_pk_fma_f32 v[232:233], v[234:235], v[234:235], v[232:233]
	v_lshlrev_b32_e32 v234, 16, v95
	v_and_b32_e32 v235, 0xffff0000, v95
	v_pk_fma_f32 v[232:233], v[234:235], v[234:235], v[232:233]
	v_lshlrev_b32_e32 v234, 16, v96
	v_and_b32_e32 v235, 0xffff0000, v96
	v_pk_fma_f32 v[232:233], v[234:235], v[234:235], v[232:233]
	v_lshlrev_b32_e32 v234, 16, v97
	v_and_b32_e32 v235, 0xffff0000, v97
	v_pk_fma_f32 v[232:233], v[234:235], v[234:235], v[232:233]
	v_lshlrev_b32_e32 v234, 16, v98
	v_and_b32_e32 v235, 0xffff0000, v98
	v_pk_fma_f32 v[232:233], v[234:235], v[234:235], v[232:233]
	v_lshlrev_b32_e32 v234, 16, v99
	v_and_b32_e32 v235, 0xffff0000, v99
	v_pk_fma_f32 v[232:233], v[234:235], v[234:235], v[232:233]
	ds_read_b128 v[200:203], v10 offset:27648
	ds_read_b128 v[204:207], v10 offset:27712
	ds_read_b128 v[208:211], v10 offset:29952
	ds_read_b128 v[212:215], v10 offset:30016
	ds_read_b128 v[216:219], v10 offset:32256
	ds_read_b128 v[220:223], v10 offset:32320
	ds_read_b128 v[224:227], v10 offset:34560
	ds_read_b128 v[228:231], v10 offset:34624
	v_add_f32_e32 v232, v232, v233
	s_nop 0
	ds_bpermute_b32 v233, v15, v232
	s_waitcnt lgkmcnt(9)
	v_mfma_f32_16x16x32_bf16 v[108:111], v[160:163], v[92:95], 0
	v_mfma_f32_16x16x32_bf16 v[112:115], v[168:171], v[92:95], 0
	v_mfma_f32_16x16x32_bf16 v[116:119], v[176:179], v[92:95], 0
	v_mfma_f32_16x16x32_bf16 v[120:123], v[184:187], v[92:95], 0
	v_mfma_f32_16x16x32_bf16 v[124:127], v[192:195], v[92:95], 0
	v_mfma_f32_16x16x32_bf16 v[108:111], v[164:167], v[96:99], v[108:111]
	v_mfma_f32_16x16x32_bf16 v[112:115], v[172:175], v[96:99], v[112:115]
	v_mfma_f32_16x16x32_bf16 v[116:119], v[180:183], v[96:99], v[116:119]
	v_mfma_f32_16x16x32_bf16 v[120:123], v[188:191], v[96:99], v[120:123]
	v_mfma_f32_16x16x32_bf16 v[124:127], v[196:199], v[96:99], v[124:127]
	s_waitcnt lgkmcnt(0)
	v_add_f32_e32 v232, v232, v233
	v_mfma_f32_16x16x32_bf16 v[128:131], v[200:203], v[92:95], 0
	v_mfma_f32_16x16x32_bf16 v[132:135], v[208:211], v[92:95], 0
	v_mfma_f32_16x16x32_bf16 v[136:139], v[216:219], v[92:95], 0
	v_mfma_f32_16x16x32_bf16 v[140:143], v[224:227], v[92:95], 0
	ds_bpermute_b32 v233, v16, v232
	v_mfma_f32_16x16x32_bf16 v[128:131], v[204:207], v[96:99], v[128:131]
	v_mfma_f32_16x16x32_bf16 v[132:135], v[212:215], v[96:99], v[132:135]
	v_mfma_f32_16x16x32_bf16 v[136:139], v[220:223], v[96:99], v[136:139]
	v_mfma_f32_16x16x32_bf16 v[140:143], v[228:231], v[96:99], v[140:143]
	ds_read2_b64 v[160:163], v11 offset0:28 offset1:32
	ds_read2_b64 v[164:167], v12 offset0:28 offset1:32
	ds_read2_b64 v[168:171], v13 offset0:28 offset1:32
	ds_read2_b64 v[172:175], v14 offset0:28 offset1:32
	ds_read2_b64 v[176:179], v11 offset0:36 offset1:40
	ds_read2_b64 v[180:183], v12 offset0:36 offset1:40
	ds_read2_b64 v[184:187], v13 offset0:36 offset1:40
	ds_read2_b64 v[188:191], v14 offset0:36 offset1:40
	ds_read2_b64 v[192:195], v11 offset0:44 offset1:48
	ds_read2_b64 v[196:199], v12 offset0:44 offset1:48
	ds_read2_b64 v[200:203], v13 offset0:44 offset1:48
	ds_read2_b64 v[204:207], v14 offset0:44 offset1:48
	s_waitcnt lgkmcnt(12)
	v_add_f32_e32 v232, v232, v233
	v_mul_f32_e32 v232, 0x3c800000, v232
	v_add_f32_e32 v232, 0x358637bd, v232
	v_rsq_f32_e32 v236, v232
	s_nop 0
	v_mov_b32_e32 v237, v236
	s_nop 1
	v_pk_fma_f32 v[108:109], v[108:109], v[236:237], v[52:53]
	v_pk_fma_f32 v[110:111], v[110:111], v[236:237], v[54:55]
	v_pk_fma_f32 v[112:113], v[112:113], v[236:237], v[56:57]
	v_pk_fma_f32 v[114:115], v[114:115], v[236:237], v[58:59]
	v_pk_fma_f32 v[116:117], v[116:117], v[236:237], v[60:61]
	v_pk_fma_f32 v[118:119], v[118:119], v[236:237], v[62:63]
	v_pk_fma_f32 v[120:121], v[120:121], v[236:237], v[64:65]
	v_pk_fma_f32 v[122:123], v[122:123], v[236:237], v[66:67]
	v_pk_fma_f32 v[124:125], v[124:125], v[236:237], v[68:69]
	v_pk_fma_f32 v[126:127], v[126:127], v[236:237], v[70:71]
	v_pk_fma_f32 v[128:129], v[128:129], v[236:237], v[72:73]
	v_pk_fma_f32 v[130:131], v[130:131], v[236:237], v[74:75]
	v_pk_fma_f32 v[132:133], v[132:133], v[236:237], v[76:77]
	v_pk_fma_f32 v[134:135], v[134:135], v[236:237], v[78:79]
	v_pk_fma_f32 v[136:137], v[136:137], v[236:237], v[80:81]
	v_pk_fma_f32 v[138:139], v[138:139], v[236:237], v[82:83]
	v_pk_fma_f32 v[140:141], v[140:141], v[236:237], v[84:85]
	v_pk_fma_f32 v[142:143], v[142:143], v[236:237], v[86:87]
	v_exp_f32_e32 v108, v108
	v_exp_f32_e32 v109, v109
	v_exp_f32_e32 v110, v110
	v_exp_f32_e32 v111, v111
	v_exp_f32_e32 v112, v112
	v_exp_f32_e32 v113, v113
	v_exp_f32_e32 v114, v114
	v_exp_f32_e32 v115, v115
	v_exp_f32_e32 v116, v116
	v_exp_f32_e32 v117, v117
	v_exp_f32_e32 v118, v118
	v_exp_f32_e32 v119, v119
	v_exp_f32_e32 v120, v120
	v_exp_f32_e32 v121, v121
	v_exp_f32_e32 v122, v122
	v_exp_f32_e32 v123, v123
	v_exp_f32_e32 v124, v124
	v_exp_f32_e32 v125, v125
	v_exp_f32_e32 v126, v126
	v_exp_f32_e32 v127, v127
	v_exp_f32_e32 v128, v128
	v_exp_f32_e32 v129, v129
	v_exp_f32_e32 v130, v130
	v_exp_f32_e32 v131, v131
	v_exp_f32_e32 v132, v132
	v_exp_f32_e32 v133, v133
	v_exp_f32_e32 v134, v134
	v_exp_f32_e32 v135, v135
	v_exp_f32_e32 v136, v136
	v_exp_f32_e32 v137, v137
	v_exp_f32_e32 v138, v138
	v_exp_f32_e32 v139, v139
	v_exp_f32_e32 v140, v140
	v_exp_f32_e32 v141, v141
	v_exp_f32_e32 v142, v142
	v_exp_f32_e32 v143, v143
	s_cmp_lg_u32 s36, 0
	s_cbranch_scc1 .Lat_m7
	v_mov_b32_e32 v108, 0
	v_mov_b32_e32 v109, 0
	v_mov_b32_e32 v110, 0
	v_mov_b32_e32 v111, 0
.Lat_m7:
	s_nop 0
	v_pk_add_f32 v[232:233], v[108:109], v[110:111]
	v_pk_add_f32 v[234:235], v[112:113], v[114:115]
	v_pk_add_f32 v[232:233], v[232:233], v[116:117]
	v_pk_add_f32 v[234:235], v[234:235], v[118:119]
	v_pk_add_f32 v[232:233], v[232:233], v[120:121]
	v_pk_add_f32 v[234:235], v[234:235], v[122:123]
	v_pk_add_f32 v[232:233], v[232:233], v[124:125]
	v_pk_add_f32 v[234:235], v[234:235], v[126:127]
	v_pk_add_f32 v[232:233], v[232:233], v[128:129]
	v_pk_add_f32 v[234:235], v[234:235], v[130:131]
	v_pk_add_f32 v[232:233], v[232:233], v[132:133]
	v_pk_add_f32 v[234:235], v[234:235], v[134:135]
	v_pk_add_f32 v[232:233], v[232:233], v[136:137]
	v_pk_add_f32 v[234:235], v[234:235], v[138:139]
	v_pk_add_f32 v[232:233], v[232:233], v[140:141]
	v_pk_add_f32 v[234:235], v[234:235], v[142:143]
	v_pk_add_f32 v[232:233], v[232:233], v[234:235]
	s_nop 0
	v_add_f32_e32 v232, v232, v233
	v_cvt_pk_bf16_f32 v108, v108, v109
	v_cvt_pk_bf16_f32 v109, v110, v111
	v_cvt_pk_bf16_f32 v110, v112, v113
	v_cvt_pk_bf16_f32 v111, v114, v115
	v_cvt_pk_bf16_f32 v116, v116, v117
	v_cvt_pk_bf16_f32 v117, v118, v119
	v_cvt_pk_bf16_f32 v118, v120, v121
	v_cvt_pk_bf16_f32 v119, v122, v123
	v_cvt_pk_bf16_f32 v124, v124, v125
	v_cvt_pk_bf16_f32 v125, v126, v127
	v_cvt_pk_bf16_f32 v126, v128, v129
	v_cvt_pk_bf16_f32 v127, v130, v131
	v_cvt_pk_bf16_f32 v132, v132, v133
	v_cvt_pk_bf16_f32 v133, v134, v135
	v_cvt_pk_bf16_f32 v134, v136, v137
	v_cvt_pk_bf16_f32 v135, v138, v139
	v_cvt_pk_bf16_f32 v140, v140, v141
	v_cvt_pk_bf16_f32 v141, v142, v143
	v_mov_b32_e32 v142, 0
	v_mov_b32_e32 v143, 0
	ds_bpermute_b32 v233, v15, v232
	s_waitcnt lgkmcnt(1)
	v_mfma_f32_16x16x32_bf16 v[144:147], v[160:163], v[108:111], 0
	v_mfma_f32_16x16x32_bf16 v[148:151], v[164:167], v[108:111], 0
	v_mfma_f32_16x16x32_bf16 v[152:155], v[168:171], v[108:111], 0
	v_mfma_f32_16x16x32_bf16 v[156:159], v[172:175], v[108:111], 0
	v_mfma_f32_16x16x32_bf16 v[144:147], v[176:179], v[116:119], v[144:147]
	v_mfma_f32_16x16x32_bf16 v[148:151], v[180:183], v[116:119], v[148:151]
	v_mfma_f32_16x16x32_bf16 v[152:155], v[184:187], v[116:119], v[152:155]
	v_mfma_f32_16x16x32_bf16 v[156:159], v[188:191], v[116:119], v[156:159]
	v_mfma_f32_16x16x32_bf16 v[144:147], v[192:195], v[124:127], v[144:147]
	v_mfma_f32_16x16x32_bf16 v[148:151], v[196:199], v[124:127], v[148:151]
	v_mfma_f32_16x16x32_bf16 v[152:155], v[200:203], v[124:127], v[152:155]
	v_mfma_f32_16x16x32_bf16 v[156:159], v[204:207], v[124:127], v[156:159]
	ds_read2_b64 v[160:163], v11 offset0:52 offset1:56
	ds_read2_b64 v[164:167], v12 offset0:52 offset1:56
	ds_read2_b64 v[168:171], v13 offset0:52 offset1:56
	ds_read2_b64 v[172:175], v14 offset0:52 offset1:56
	ds_read2_b64 v[176:179], v11 offset0:60 offset1:60
	ds_read2_b64 v[180:183], v12 offset0:60 offset1:60
	ds_read2_b64 v[184:187], v13 offset0:60 offset1:60
	ds_read2_b64 v[188:191], v14 offset0:60 offset1:60
	s_waitcnt lgkmcnt(8)
	v_add_f32_e32 v232, v232, v233
	s_nop 0
	ds_bpermute_b32 v233, v16, v232
	s_waitcnt lgkmcnt(1)
	v_mfma_f32_16x16x32_bf16 v[144:147], v[160:163], v[132:135], v[144:147]
	v_mfma_f32_16x16x32_bf16 v[148:151], v[164:167], v[132:135], v[148:151]
	v_mfma_f32_16x16x32_bf16 v[152:155], v[168:171], v[132:135], v[152:155]
	v_mfma_f32_16x16x32_bf16 v[156:159], v[172:175], v[132:135], v[156:159]
	v_mfma_f32_16x16x32_bf16 v[144:147], v[176:179], v[140:143], v[144:147]
	v_mfma_f32_16x16x32_bf16 v[148:151], v[180:183], v[140:143], v[148:151]
	v_mfma_f32_16x16x32_bf16 v[152:155], v[184:187], v[140:143], v[152:155]
	v_mfma_f32_16x16x32_bf16 v[156:159], v[188:191], v[140:143], v[156:159]
	s_waitcnt lgkmcnt(0)
	v_add_f32_e32 v232, v232, v233
	v_add_f32_e32 v232, v232, v88
	v_rcp_f32_e32 v236, v232
	s_nop 0
	v_mov_b32_e32 v237, v236
	s_nop 4
	v_pk_mul_f32 v[144:145], v[144:145], v[236:237]
	v_pk_mul_f32 v[146:147], v[146:147], v[236:237]
	v_pk_mul_f32 v[148:149], v[148:149], v[236:237]
	v_pk_mul_f32 v[150:151], v[150:151], v[236:237]
	v_pk_mul_f32 v[152:153], v[152:153], v[236:237]
	v_pk_mul_f32 v[154:155], v[154:155], v[236:237]
	v_pk_mul_f32 v[156:157], v[156:157], v[236:237]
	v_pk_mul_f32 v[158:159], v[158:159], v[236:237]
	v_cvt_pk_bf16_f32 v144, v144, v145
	v_cvt_pk_bf16_f32 v145, v146, v147
	v_cvt_pk_bf16_f32 v148, v148, v149
	v_cvt_pk_bf16_f32 v149, v150, v151
	v_cvt_pk_bf16_f32 v152, v152, v153
	v_cvt_pk_bf16_f32 v153, v154, v155
	v_cvt_pk_bf16_f32 v156, v156, v157
	v_cvt_pk_bf16_f32 v157, v158, v159
	global_store_dwordx2 v9, v[144:145], s[50:51] offset:0
	global_store_dwordx2 v9, v[148:149], s[50:51] offset:32
	global_store_dwordx2 v9, v[152:153], s[50:51] offset:64
	global_store_dwordx2 v9, v[156:157], s[50:51] offset:96
	s_mov_b32 s34, s39
	s_cmpk_gt_u32 s34, 0x3ff
	s_cbranch_scc0 .Lat_item
.Lat_done:
.LBB0_1473:
	s_cmp_gt_i32 s47, 15
	s_cselect_b64 s[6:7], -1, 0
	s_and_b64 s[2:3], s[28:29], s[6:7]
	s_andn2_b64 vcc, exec, s[2:3]
	s_cbranch_vccnz .LBB0_1527
	s_waitcnt vmcnt(0)
	s_waitcnt vmcnt(0) lgkmcnt(0)
	s_barrier
	s_mov_b64 s[8:9], exec
	v_readlane_b32 s2, v252, 5
	v_readlane_b32 s3, v252, 6
	s_and_b64 s[2:3], s[8:9], s[2:3]
	s_mov_b64 exec, s[2:3]
	s_cbranch_execz .LBB0_1526
	s_add_i32 s2, 0, 0x24c40
	v_mov_b32_e32 v1, s2
	s_waitcnt vmcnt(0) expcnt(0) lgkmcnt(0)
	ds_read_b32 v3, v1
	s_add_i32 s2, 0, 0x24c44
	v_mov_b32_e32 v1, s2
	ds_read_b32 v1, v1
	s_waitcnt lgkmcnt(1)
	v_cmp_ne_u32_e32 vcc, 0, v3
	s_cbranch_vccnz .LBB0_1490
	s_add_u32 s10, s44, 0x4200
	s_addc_u32 s11, s45, 0
	s_add_u32 s12, s44, 0x4400
	s_addc_u32 s13, s45, 0
	s_add_u32 s14, s44, 0x4500
	s_addc_u32 s15, s45, 0
	s_add_u32 s16, s44, 0x4600
	s_addc_u32 s17, s45, 0
	s_add_u32 s18, s44, 0x4700
	s_addc_u32 s19, s45, 0
	s_add_u32 s20, s44, 0x4800
	s_addc_u32 s21, s45, 0
	s_add_u32 s22, s44, 0x4900
	s_addc_u32 s23, s45, 0
	s_add_u32 s24, s44, 0x4a00
	s_addc_u32 s25, s45, 0
	s_add_u32 s26, s44, 0x4b00
	s_addc_u32 s27, s45, 0
	s_add_u32 s28, s44, 0x4c00
	s_addc_u32 s29, s45, 0
	s_add_u32 s30, s44, 0x4d00
	s_addc_u32 s31, s45, 0
	s_add_u32 s34, s44, 0x4e00
	s_addc_u32 s35, s45, 0
	s_add_u32 s36, s44, 0x4f00
	v_readlane_b32 s4, v252, 0
	s_addc_u32 s37, s45, 0
	v_readlane_b32 s5, v252, 1
	s_add_u32 s38, s44, 0x5000
	s_load_dwordx2 s[2:3], s[4:5], 0x4
	s_addc_u32 s39, s45, 0
	s_add_u32 s40, s44, 0x5100
	s_addc_u32 s41, s45, 0
	s_add_u32 s54, s44, 0x5200
	s_addc_u32 s55, s45, 0
	s_waitcnt lgkmcnt(0)
	s_mul_i32 s2, s2, s91
	s_add_u32 s56, s44, 0x5300
	s_mul_i32 s2, s2, s3
	s_addc_u32 s57, s45, 0
	s_mov_b32 s3, 1
	v_mov_b32_e32 v17, 0
	s_branch .LBB0_1478
